# split phase-B loop body into two sequential halves; softmax lane exchanges via permlane swaps
# speedup vs baseline: 1.0012x; 1.0012x over previous
_Z12fused_kernelPKfS0_Pf:
	s_load_dwordx4 s[12:15], s[0:1], 0x0
	s_load_dwordx2 s[8:9], s[0:1], 0x10
	s_lshl_b32 s0, s2, 5
	s_and_b32 s0, s0, 0xe0
	s_lshr_b32 s3, s2, 3
	s_add_i32 s0, s0, s3
	v_and_b32_e32 v1, 63, v0
	v_lshrrev_b32_e32 v200, 6, v0
	s_lshl_b32 s0, s0, 17
	v_lshlrev_b32_e32 v194, 4, v0
	v_lshl_add_u32 v2, v200, 25, s0
	v_lshlrev_b32_e32 v198, 4, v1
	v_add_u32_e32 v106, 0x2000, v194
	v_add_u32_e32 v107, 0x4000, v194
	v_or_b32_e32 v203, v2, v198
	v_lshlrev_b32_e32 v196, 10, v200
	v_mov_b32_e32 v195, 0
	v_or_b32_e32 v233, v203, v196
	s_mov_b32 s7, 0x20000
	s_brev_b32 s6, 8
	s_waitcnt lgkmcnt(0)
	global_load_dwordx4 v[228:231], v194, s[14:15]
	global_load_dwordx4 v[98:101], v106, s[14:15]
	global_load_dwordx4 v[102:105], v107, s[14:15]
	v_add_u32_e32 v107, 0x6000, v194
	global_load_dwordx4 v[116:119], v107, s[14:15]
	v_add_u32_e32 v106, 0x8000, v194
	global_load_dwordx4 v[120:123], v106, s[14:15]
	v_add_u32_e32 v107, 0xa000, v194
	global_load_dwordx4 v[124:127], v107, s[14:15]
	v_add_u32_e32 v106, 0xc000, v194
	global_load_dwordx4 v[128:131], v106, s[14:15]
	v_add_u32_e32 v107, 0xe000, v194
	global_load_dwordx4 v[132:135], v107, s[14:15]
	v_add_u32_e32 v106, 0x10000, v194
	global_load_dwordx4 v[136:139], v106, s[14:15]
	v_add_u32_e32 v107, 0x12000, v194
	global_load_dwordx4 v[140:143], v107, s[14:15]
	v_add_u32_e32 v106, 0x14000, v194
	global_load_dwordx4 v[158:161], v106, s[14:15]
	v_add_u32_e32 v107, 0x16000, v194
	global_load_dwordx4 v[170:173], v107, s[14:15]
	v_add_u32_e32 v106, 0x18000, v194
	global_load_dwordx4 v[186:189], v106, s[14:15]
	v_add_u32_e32 v107, 0x1a000, v194
	global_load_dwordx4 v[190:193], v107, s[14:15]
	v_add_u32_e32 v106, 0x1c000, v194
	global_load_dwordx4 v[204:207], v106, s[14:15]
	v_add_u32_e32 v107, 0x1e000, v194
	global_load_dwordx4 v[208:211], v107, s[14:15]
	v_add_u32_e32 v106, 0x20000, v194
	global_load_dwordx4 v[212:215], v106, s[14:15]
	v_add_u32_e32 v107, 0x22000, v194
	global_load_dwordx4 v[216:219], v107, s[14:15]
	v_add_u32_e32 v106, 0x24000, v194
	global_load_dwordx4 v[220:223], v106, s[14:15]
	v_add_u32_e32 v107, 0x26000, v194
	global_load_dwordx4 v[112:115], v107, s[14:15]
	s_and_b32 s5, s13, 0xffff
	s_mov_b32 s4, s12
	buffer_load_dwordx4 v[70:73], v233, s[4:7], 0 offen nt
	v_or_b32_e32 v107, 0x2000, v233
	buffer_load_dwordx4 v[66:69], v107, s[4:7], 0 offen nt
	v_or_b32_e32 v106, 0x4000, v233
	buffer_load_dwordx4 v[78:81], v106, s[4:7], 0 offen nt
	v_or_b32_e32 v107, 0x6000, v233
	buffer_load_dwordx4 v[74:77], v107, s[4:7], 0 offen nt
	v_or_b32_e32 v106, 0x8000, v233
	buffer_load_dwordx4 v[86:89], v106, s[4:7], 0 offen nt
	v_or_b32_e32 v107, 0xa000, v233
	buffer_load_dwordx4 v[82:85], v107, s[4:7], 0 offen nt
	v_or_b32_e32 v106, 0xc000, v233
	buffer_load_dwordx4 v[94:97], v106, s[4:7], 0 offen nt
	v_or_b32_e32 v107, 0xe000, v233
	buffer_load_dwordx4 v[90:93], v107, s[4:7], 0 offen nt
	v_or_b32_e32 v106, 0x10000, v233
	buffer_load_dwordx4 v[150:153], v106, s[4:7], 0 offen nt
	v_or_b32_e32 v107, 0x12000, v233
	buffer_load_dwordx4 v[146:149], v107, s[4:7], 0 offen nt
	v_or_b32_e32 v106, 0x14000, v233
	buffer_load_dwordx4 v[162:165], v106, s[4:7], 0 offen nt
	v_or_b32_e32 v107, 0x16000, v233
	buffer_load_dwordx4 v[154:157], v107, s[4:7], 0 offen nt
	v_or_b32_e32 v106, 0x18000, v233
	buffer_load_dwordx4 v[174:177], v106, s[4:7], 0 offen nt
	v_or_b32_e32 v107, 0x1a000, v233
	buffer_load_dwordx4 v[166:169], v107, s[4:7], 0 offen nt
	v_or_b32_e32 v106, 0x1c000, v233
	buffer_load_dwordx4 v[182:185], v106, s[4:7], 0 offen nt
	v_or_b32_e32 v107, 0x1e000, v233
	buffer_load_dwordx4 v[178:181], v107, s[4:7], 0 offen nt
	v_add_u32_e32 v224, 0x400, v196
	s_movk_i32 s0, 0x1c00
	v_and_or_b32 v224, v224, s0, v203
	buffer_load_dwordx4 v[62:65], v224, s[4:7], 0 offen nt
	v_or_b32_e32 v107, 0x2000, v224
	buffer_load_dwordx4 v[38:41], v107, s[4:7], 0 offen nt
	v_or_b32_e32 v106, 0x4000, v224
	buffer_load_dwordx4 v[42:45], v106, s[4:7], 0 offen nt
	v_or_b32_e32 v107, 0x6000, v224
	buffer_load_dwordx4 v[14:17], v107, s[4:7], 0 offen nt
	v_or_b32_e32 v106, 0x8000, v224
	buffer_load_dwordx4 v[46:49], v106, s[4:7], 0 offen nt
	v_or_b32_e32 v107, 0xa000, v224
	buffer_load_dwordx4 v[18:21], v107, s[4:7], 0 offen nt
	v_or_b32_e32 v106, 0xc000, v224
	buffer_load_dwordx4 v[50:53], v106, s[4:7], 0 offen nt
	v_or_b32_e32 v107, 0xe000, v224
	buffer_load_dwordx4 v[22:25], v107, s[4:7], 0 offen nt
	v_or_b32_e32 v106, 0x10000, v224
	buffer_load_dwordx4 v[54:57], v106, s[4:7], 0 offen nt
	v_or_b32_e32 v107, 0x12000, v224
	buffer_load_dwordx4 v[26:29], v107, s[4:7], 0 offen nt
	v_or_b32_e32 v106, 0x14000, v224
	buffer_load_dwordx4 v[58:61], v106, s[4:7], 0 offen nt
	v_or_b32_e32 v107, 0x16000, v224
	buffer_load_dwordx4 v[30:33], v107, s[4:7], 0 offen nt
	v_or_b32_e32 v106, 0x18000, v224
	buffer_load_dwordx4 v[34:37], v106, s[4:7], 0 offen nt
	v_or_b32_e32 v107, 0x1a000, v224
	buffer_load_dwordx4 v[6:9], v107, s[4:7], 0 offen nt
	v_or_b32_e32 v106, 0x1c000, v224
	buffer_load_dwordx4 v[10:13], v106, s[4:7], 0 offen nt
	v_or_b32_e32 v107, 0x1e000, v224
	buffer_load_dwordx4 v[2:5], v107, s[4:7], 0 offen nt
	s_mov_b32 s1, 0xe000
	s_mov_b32 s10, 0xa000
	s_mov_b32 s11, 0x6000
	s_mov_b32 s12, 0xc000
	s_mov_b32 s13, 0x8000
	s_mov_b32 s14, 0x1e000
	s_mov_b32 s15, 0x1c000
	s_mov_b32 s16, 0x2000
	s_mov_b32 s17, 0x4000
	s_mov_b32 s18, 0x10000
	s_mov_b32 s19, 0x1a000
	s_mov_b32 s20, 0x18000
	s_mov_b32 s21, 0x16000
	s_mov_b32 s22, 0x14000
	s_mov_b32 s23, 0x12000
	s_mov_b32 s24, 0xe0
	s_mov_b32 s26, 0x3e13bb63
	v_lshrrev_b32_e32 v144, 3, v0
	v_bfe_u32 v145, v0, 1, 2
	v_lshlrev_b32_e32 v108, 3, v0
	v_and_b32_e32 v109, 8, v108
	v_lshlrev_b32_e32 v224, 8, v144
	v_lshlrev_b32_e32 v225, 6, v145
	v_lshlrev_b32_e32 v226, 8, v145
	v_lshlrev_b32_e32 v110, 10, v144
	v_or3_b32 v110, v226, v110, v109
	v_or3_b32 v111, v224, v225, v109
	v_add_u32_e32 v111, 0xff00, v111
	v_add_u32_e32 v144, 0x24800, v194
	v_bfe_u32 v201, v0, 4, 2
	v_and_b32_e32 v197, 15, v0
	v_lshlrev_b32_e32 v202, 2, v201
	s_waitcnt vmcnt(50)
	v_pk_add_f32 v[224:225], v[228:229], 0 op_sel_hi:[1,0]
	v_pk_add_f32 v[226:227], v[230:231], 0 op_sel_hi:[1,0]
	v_cvt_pk_bf16_f32 v228, v228, v229
	v_cvt_pk_bf16_f32 v229, v230, v231
	v_pk_add_f32 v[224:225], v[224:225], v[98:99]
	v_pk_add_f32 v[226:227], v[226:227], v[100:101]
	v_cvt_pk_bf16_f32 v98, v98, v99
	v_cvt_pk_bf16_f32 v99, v100, v101
	ds_write2_b64 v110, v[228:229], v[98:99] offset1:2
	s_waitcnt vmcnt(48)
	v_pk_add_f32 v[224:225], v[224:225], v[102:103]
	v_pk_add_f32 v[226:227], v[226:227], v[104:105]
	v_cvt_pk_bf16_f32 v102, v102, v103
	v_cvt_pk_bf16_f32 v103, v104, v105
	v_pk_add_f32 v[224:225], v[224:225], v[116:117]
	v_pk_add_f32 v[226:227], v[226:227], v[118:119]
	v_cvt_pk_bf16_f32 v116, v116, v117
	v_cvt_pk_bf16_f32 v117, v118, v119
	ds_write2_b64 v110, v[102:103], v[116:117] offset0:4 offset1:6
	s_waitcnt vmcnt(46)
	v_pk_add_f32 v[224:225], v[224:225], v[120:121]
	v_pk_add_f32 v[226:227], v[226:227], v[122:123]
	v_cvt_pk_bf16_f32 v120, v120, v121
	v_cvt_pk_bf16_f32 v121, v122, v123
	v_pk_add_f32 v[224:225], v[224:225], v[124:125]
	v_pk_add_f32 v[226:227], v[226:227], v[126:127]
	v_cvt_pk_bf16_f32 v124, v124, v125
	v_cvt_pk_bf16_f32 v125, v126, v127
	ds_write2_b64 v110, v[120:121], v[124:125] offset0:8 offset1:10
	s_waitcnt vmcnt(44)
	v_pk_add_f32 v[224:225], v[224:225], v[128:129]
	v_pk_add_f32 v[226:227], v[226:227], v[130:131]
	v_cvt_pk_bf16_f32 v128, v128, v129
	v_cvt_pk_bf16_f32 v129, v130, v131
	v_pk_add_f32 v[224:225], v[224:225], v[132:133]
	v_pk_add_f32 v[226:227], v[226:227], v[134:135]
	v_cvt_pk_bf16_f32 v132, v132, v133
	v_cvt_pk_bf16_f32 v133, v134, v135
	ds_write2_b64 v110, v[128:129], v[132:133] offset0:12 offset1:14
	s_waitcnt vmcnt(42)
	v_pk_add_f32 v[224:225], v[224:225], v[136:137]
	v_pk_add_f32 v[226:227], v[226:227], v[138:139]
	v_cvt_pk_bf16_f32 v136, v136, v137
	v_cvt_pk_bf16_f32 v137, v138, v139
	v_pk_add_f32 v[224:225], v[224:225], v[140:141]
	v_pk_add_f32 v[226:227], v[226:227], v[142:143]
	v_cvt_pk_bf16_f32 v140, v140, v141
	v_cvt_pk_bf16_f32 v141, v142, v143
	ds_write2_b64 v110, v[136:137], v[140:141] offset0:16 offset1:18
	s_waitcnt vmcnt(40)
	v_pk_add_f32 v[224:225], v[224:225], v[158:159]
	v_pk_add_f32 v[226:227], v[226:227], v[160:161]
	v_cvt_pk_bf16_f32 v158, v158, v159
	v_cvt_pk_bf16_f32 v159, v160, v161
	v_pk_add_f32 v[224:225], v[224:225], v[170:171]
	v_pk_add_f32 v[226:227], v[226:227], v[172:173]
	v_cvt_pk_bf16_f32 v170, v170, v171
	v_cvt_pk_bf16_f32 v171, v172, v173
	ds_write2_b64 v110, v[158:159], v[170:171] offset0:20 offset1:22
	s_waitcnt vmcnt(38)
	v_pk_add_f32 v[224:225], v[224:225], v[186:187]
	v_pk_add_f32 v[226:227], v[226:227], v[188:189]
	v_cvt_pk_bf16_f32 v186, v186, v187
	v_cvt_pk_bf16_f32 v187, v188, v189
	v_pk_add_f32 v[224:225], v[224:225], v[190:191]
	v_pk_add_f32 v[226:227], v[226:227], v[192:193]
	v_cvt_pk_bf16_f32 v190, v190, v191
	v_cvt_pk_bf16_f32 v191, v192, v193
	ds_write2_b64 v110, v[186:187], v[190:191] offset0:24 offset1:26
	s_waitcnt vmcnt(36)
	v_pk_add_f32 v[224:225], v[224:225], v[204:205]
	v_pk_add_f32 v[226:227], v[226:227], v[206:207]
	v_cvt_pk_bf16_f32 v204, v204, v205
	v_cvt_pk_bf16_f32 v205, v206, v207
	v_pk_add_f32 v[224:225], v[224:225], v[208:209]
	v_pk_add_f32 v[226:227], v[226:227], v[210:211]
	v_cvt_pk_bf16_f32 v208, v208, v209
	v_cvt_pk_bf16_f32 v209, v210, v211
	ds_write2_b64 v110, v[204:205], v[208:209] offset0:28 offset1:30
	s_waitcnt vmcnt(34)
	v_pk_add_f32 v[224:225], v[224:225], v[212:213]
	v_pk_add_f32 v[226:227], v[226:227], v[214:215]
	v_cvt_pk_bf16_f32 v212, v212, v213
	v_cvt_pk_bf16_f32 v213, v214, v215
	v_pk_add_f32 v[224:225], v[224:225], v[216:217]
	v_pk_add_f32 v[226:227], v[226:227], v[218:219]
	v_cvt_pk_bf16_f32 v216, v216, v217
	v_cvt_pk_bf16_f32 v217, v218, v219
	ds_write2_b64 v111, v[212:213], v[216:217] offset0:32 offset1:34
	s_waitcnt vmcnt(32)
	v_pk_add_f32 v[224:225], v[224:225], v[220:221]
	v_pk_add_f32 v[226:227], v[226:227], v[222:223]
	v_cvt_pk_bf16_f32 v220, v220, v221
	v_cvt_pk_bf16_f32 v221, v222, v223
	v_pk_add_f32 v[224:225], v[224:225], v[112:113]
	v_pk_add_f32 v[226:227], v[226:227], v[114:115]
	v_cvt_pk_bf16_f32 v112, v112, v113
	v_cvt_pk_bf16_f32 v113, v114, v115
	ds_write2_b64 v111, v[220:221], v[112:113] offset0:36 offset1:38
	v_pk_mul_f32 v[224:225], v[224:225], s[26:27] op_sel_hi:[1,0]
	v_pk_mul_f32 v[226:227], v[226:227], s[26:27] op_sel_hi:[1,0]
	ds_write_b128 v144, v[224:227]
	v_and_or_b32 v98, v0, 3, v202
	v_mov_b32_e32 v99, 0x10000
	v_lshl_or_b32 v204, v98, 4, v99
	s_movk_i32 s25, 0x2100
	v_mov_b32_e32 v98, 0x14000
	v_mad_u32_u24 v199, v200, s25, v98
	v_add_u32_e32 v98, 0x800, v196
	v_and_or_b32 v186, v98, s0, v203
	v_or_b32_e32 v98, 0x2000, v186
	s_waitcnt lgkmcnt(0)
	s_barrier
	buffer_load_dwordx4 v[102:105], v186, s[4:7], 0 offen nt
	s_nop 0
	buffer_load_dwordx4 v[98:101], v98, s[4:7], 0 offen nt
	v_or_b32_e32 v106, 0x4000, v186
	v_or_b32_e32 v107, 0x6000, v186
	v_or_b32_e32 v114, 0x8000, v186
	v_or_b32_e32 v115, 0xa000, v186
	v_or_b32_e32 v122, 0xc000, v186
	v_or_b32_e32 v123, 0xe000, v186
	v_or_b32_e32 v130, 0x10000, v186
	v_or_b32_e32 v131, 0x12000, v186
	v_or_b32_e32 v138, 0x14000, v186
	v_or_b32_e32 v139, 0x16000, v186
	v_or_b32_e32 v158, 0x18000, v186
	v_or_b32_e32 v159, 0x1a000, v186
	v_or_b32_e32 v187, 0x1c000, v186
	v_or_b32_e32 v186, 0x1e000, v186
	v_or_b32_e32 v213, v199, v109
	v_and_b32_e32 v214, 0x1f0, v108
	buffer_load_dwordx4 v[110:113], v106, s[4:7], 0 offen nt
	s_nop 0
	buffer_load_dwordx4 v[106:109], v107, s[4:7], 0 offen nt
	s_nop 0
	buffer_load_dwordx4 v[118:121], v114, s[4:7], 0 offen nt
	s_nop 0
	buffer_load_dwordx4 v[114:117], v115, s[4:7], 0 offen nt
	s_nop 0
	buffer_load_dwordx4 v[126:129], v122, s[4:7], 0 offen nt
	s_nop 0
	buffer_load_dwordx4 v[122:125], v123, s[4:7], 0 offen nt
	s_nop 0
	buffer_load_dwordx4 v[134:137], v130, s[4:7], 0 offen nt
	s_nop 0
	buffer_load_dwordx4 v[130:133], v131, s[4:7], 0 offen nt
	s_nop 0
	buffer_load_dwordx4 v[142:145], v138, s[4:7], 0 offen nt
	s_nop 0
	buffer_load_dwordx4 v[138:141], v139, s[4:7], 0 offen nt
	s_nop 0
	buffer_load_dwordx4 v[170:173], v158, s[4:7], 0 offen nt
	s_nop 0
	buffer_load_dwordx4 v[158:161], v159, s[4:7], 0 offen nt
	s_nop 0
	buffer_load_dwordx4 v[190:193], v187, s[4:7], 0 offen nt
	s_nop 0
	buffer_load_dwordx4 v[186:189], v186, s[4:7], 0 offen nt
	s_waitcnt vmcnt(32)
	v_cvt_pk_bf16_f32 v66, v66, v67
	v_cvt_pk_bf16_f32 v67, v68, v69
	s_movk_i32 s25, 0x50
	v_xad_u32 v207, v214, s25, v213
	s_movk_i32 s25, 0x60
	v_xad_u32 v206, v214, s25, v213
	s_movk_i32 s25, 0x70
	v_xad_u32 v205, v214, s25, v213
	s_movk_i32 s25, 0x80
	v_xad_u32 v211, v214, 16, v213
	v_xad_u32 v231, v214, s25, v213
	s_movk_i32 s25, 0x90
	v_xad_u32 v210, v214, 32, v213
	v_xad_u32 v230, v214, s25, v213
	s_movk_i32 s25, 0xa0
	ds_write_b64 v211, v[66:67] offset:512
	v_cvt_pk_bf16_f32 v66, v78, v79
	v_cvt_pk_bf16_f32 v67, v80, v81
	v_xad_u32 v209, v214, 48, v213
	v_xad_u32 v229, v214, s25, v213
	s_movk_i32 s25, 0xb0
	ds_write_b64 v210, v[66:67] offset:1024
	v_cvt_pk_bf16_f32 v66, v74, v75
	v_cvt_pk_bf16_f32 v67, v76, v77
	v_xad_u32 v208, v214, 64, v213
	v_xad_u32 v228, v214, s25, v213
	s_movk_i32 s25, 0xc0
	ds_write_b64 v209, v[66:67] offset:1536
	v_cvt_pk_bf16_f32 v66, v86, v87
	v_cvt_pk_bf16_f32 v67, v88, v89
	v_xad_u32 v227, v214, s25, v213
	s_movk_i32 s25, 0xd0
	v_xad_u32 v225, v214, s24, v213
	s_movk_i32 s24, 0xf0
	ds_write_b64 v208, v[66:67] offset:2048
	v_cvt_pk_bf16_f32 v66, v82, v83
	v_cvt_pk_bf16_f32 v67, v84, v85
	v_add_u32_e32 v212, v213, v214
	v_xad_u32 v226, v214, s25, v213
	v_xad_u32 v224, v214, s24, v213
	v_lshl_add_u32 v213, v197, 9, v199
	v_bitop3_b32 v214, v201, v0, 15 bitop3:0x78
	ds_write_b64 v207, v[66:67] offset:2560
	v_cvt_pk_bf16_f32 v66, v94, v95
	v_cvt_pk_bf16_f32 v67, v96, v97
	v_lshl_or_b32 v223, v214, 4, v213
	v_bitop3_b32 v214, v201, v197, 4 bitop3:0x36
	ds_write_b64 v206, v[66:67] offset:3072
	v_cvt_pk_bf16_f32 v66, v90, v91
	v_cvt_pk_bf16_f32 v67, v92, v93
	v_lshl_or_b32 v222, v214, 4, v213
	v_bitop3_b32 v214, v201, v197, 8 bitop3:0x36
	ds_write_b64 v205, v[66:67] offset:3584
	v_cvt_pk_bf16_f32 v66, v150, v151
	v_cvt_pk_bf16_f32 v67, v152, v153
	v_lshl_or_b32 v221, v214, 4, v213
	v_bitop3_b32 v214, v201, v197, 12 bitop3:0x36
	ds_write_b64 v231, v[66:67] offset:4096
	v_cvt_pk_bf16_f32 v66, v146, v147
	v_cvt_pk_bf16_f32 v67, v148, v149
	v_lshl_or_b32 v219, v214, 4, v213
	v_bitop3_b32 v214, v201, v197, 16 bitop3:0x36
	ds_write_b64 v230, v[66:67] offset:4608
	v_cvt_pk_bf16_f32 v66, v162, v163
	v_cvt_pk_bf16_f32 v67, v164, v165
	v_lshl_add_u32 v218, v214, 4, v213
	v_bitop3_b32 v214, v201, v197, 20 bitop3:0x36
	ds_write_b64 v229, v[66:67] offset:5120
	v_cvt_pk_bf16_f32 v66, v154, v155
	v_cvt_pk_bf16_f32 v67, v156, v157
	v_lshl_add_u32 v217, v214, 4, v213
	v_bitop3_b32 v214, v201, v197, 24 bitop3:0x36
	ds_write_b64 v228, v[66:67] offset:5632
	v_cvt_pk_bf16_f32 v66, v174, v175
	v_cvt_pk_bf16_f32 v67, v176, v177
	v_lshl_add_u32 v216, v214, 4, v213
	v_bitop3_b32 v214, v201, v197, 28 bitop3:0x36
	ds_write_b64 v227, v[66:67] offset:6144
	v_cvt_pk_bf16_f32 v66, v166, v167
	v_cvt_pk_bf16_f32 v67, v168, v169
	v_add_u32_e32 v235, 3, v200
	v_lshl_add_u32 v213, v214, 4, v213
	ds_write_b64 v226, v[66:67] offset:6656
	v_cvt_pk_bf16_f32 v66, v182, v183
	v_cvt_pk_bf16_f32 v67, v184, v185
	v_cvt_pk_bf16_f32 v70, v70, v71
	v_cvt_pk_bf16_f32 v71, v72, v73
	ds_write_b64 v212, v[70:71]
	ds_write_b64 v225, v[66:67] offset:7168
	v_cvt_pk_bf16_f32 v66, v178, v179
	v_cvt_pk_bf16_f32 v67, v180, v181
	ds_write_b64 v224, v[66:67] offset:7680
	v_lshl_or_b32 v66, v200, 13, v198
	ds_read_b128 v[66:69], v66
	v_lshlrev_b32_e32 v220, 11, v200
	v_or_b32_e32 v70, v204, v220
	ds_read_b128 v[70:73], v70
	ds_read_b128 v[74:77], v223
	v_lshlrev_b32_e32 v232, 3, v200
	v_or_b32_e32 v214, 1, v232
	s_waitcnt lgkmcnt(0)
	v_mfma_f32_16x16x32_bf16 v[70:73], v[70:73], v[74:77], 0
	v_lshlrev_b32_e32 v215, 8, v214
	v_or_b32_e32 v78, v204, v215
	v_or_b32_e32 v184, 2, v232
	v_mfma_f32_16x16x32_bf16 v[66:69], v[66:69], v[74:77], 0
	v_lshl_or_b32 v74, v214, 10, v198
	ds_read_b128 v[74:77], v74
	ds_read_b128 v[78:81], v78
	ds_read_b128 v[82:85], v222
	v_lshlrev_b32_e32 v185, 8, v184
	s_waitcnt lgkmcnt(0)
	v_mfma_f32_16x16x32_bf16 v[70:73], v[78:81], v[82:85], v[70:73]
	v_or_b32_e32 v78, v204, v185
	v_or_b32_e32 v182, 3, v232
	v_lshlrev_b32_e32 v183, 8, v182
	v_mfma_f32_16x16x32_bf16 v[66:69], v[74:77], v[82:85], v[66:69]
	v_lshl_or_b32 v74, v184, 10, v198
	ds_read_b128 v[74:77], v74
	ds_read_b128 v[78:81], v78
	ds_read_b128 v[82:85], v221
	s_waitcnt lgkmcnt(0)
	v_mfma_f32_16x16x32_bf16 v[70:73], v[78:81], v[82:85], v[70:73]
	v_or_b32_e32 v78, v204, v183
	v_or_b32_e32 v180, 4, v232
	v_lshlrev_b32_e32 v181, 8, v180
	v_mfma_f32_16x16x32_bf16 v[66:69], v[74:77], v[82:85], v[66:69]
	v_lshl_or_b32 v74, v182, 10, v198
	ds_read_b128 v[74:77], v74
	ds_read_b128 v[78:81], v78
	ds_read_b128 v[82:85], v219
	s_waitcnt lgkmcnt(0)
	v_mfma_f32_16x16x32_bf16 v[66:69], v[74:77], v[82:85], v[66:69]
	v_lshl_or_b32 v74, v180, 10, v198
	ds_read_b128 v[74:77], v74
	v_or_b32_e32 v178, 5, v232
	v_mfma_f32_16x16x32_bf16 v[70:73], v[78:81], v[82:85], v[70:73]
	v_or_b32_e32 v78, v204, v181
	ds_read_b128 v[78:81], v78
	ds_read_b128 v[82:85], v218
	v_lshlrev_b32_e32 v179, 8, v178
	s_waitcnt lgkmcnt(0)
	v_mfma_f32_16x16x32_bf16 v[66:69], v[74:77], v[82:85], v[66:69]
	v_lshl_or_b32 v74, v178, 10, v198
	ds_read_b128 v[74:77], v74
	v_or_b32_e32 v176, 6, v232
	v_mfma_f32_16x16x32_bf16 v[70:73], v[78:81], v[82:85], v[70:73]
	v_or_b32_e32 v78, v204, v179
	ds_read_b128 v[78:81], v78
	ds_read_b128 v[82:85], v217
	v_lshlrev_b32_e32 v177, 8, v176
	s_waitcnt lgkmcnt(0)
	v_mfma_f32_16x16x32_bf16 v[66:69], v[74:77], v[82:85], v[66:69]
	v_lshl_or_b32 v74, v176, 10, v198
	ds_read_b128 v[74:77], v74
	v_or_b32_e32 v174, 7, v232
	v_mfma_f32_16x16x32_bf16 v[70:73], v[78:81], v[82:85], v[70:73]
	v_or_b32_e32 v78, v204, v177
	ds_read_b128 v[78:81], v78
	ds_read_b128 v[82:85], v216
	v_lshlrev_b32_e32 v175, 8, v174
	s_waitcnt lgkmcnt(0)
	v_mfma_f32_16x16x32_bf16 v[66:69], v[74:77], v[82:85], v[66:69]
	v_lshl_or_b32 v74, v174, 10, v198
	s_waitcnt vmcnt(16)
	v_cvt_pk_bf16_f32 v14, v14, v15
	v_cvt_pk_bf16_f32 v15, v16, v17
	v_mfma_f32_16x16x32_bf16 v[70:73], v[78:81], v[82:85], v[70:73]
	v_or_b32_e32 v78, v204, v175
	ds_read_b128 v[74:77], v74
	ds_read_b128 v[78:81], v78
	ds_read_b128 v[82:85], v213
	ds_write_b64 v209, v[14:15] offset:1536
	v_cvt_pk_bf16_f32 v14, v46, v47
	v_cvt_pk_bf16_f32 v15, v48, v49
	ds_write_b64 v208, v[14:15] offset:2048
	v_cvt_pk_bf16_f32 v14, v18, v19
	v_cvt_pk_bf16_f32 v15, v20, v21
	ds_write_b64 v207, v[14:15] offset:2560
	v_cvt_pk_bf16_f32 v14, v50, v51
	v_cvt_pk_bf16_f32 v15, v52, v53
	ds_write_b64 v206, v[14:15] offset:3072
	v_cvt_pk_bf16_f32 v14, v22, v23
	v_cvt_pk_bf16_f32 v15, v24, v25
	ds_write_b64 v205, v[14:15] offset:3584
	v_cvt_pk_bf16_f32 v14, v54, v55
	v_cvt_pk_bf16_f32 v15, v56, v57
	v_cvt_pk_bf16_f32 v6, v6, v7
	v_cvt_pk_bf16_f32 v2, v2, v3
	ds_write_b64 v231, v[14:15] offset:4096
	v_cvt_pk_bf16_f32 v14, v26, v27
	v_cvt_pk_bf16_f32 v15, v28, v29
	v_cvt_pk_bf16_f32 v7, v8, v9
	ds_write_b64 v226, v[6:7] offset:6656
	v_cvt_pk_bf16_f32 v6, v10, v11
	v_cvt_pk_bf16_f32 v3, v4, v5
	ds_write_b64 v224, v[2:3] offset:7680
	v_lshlrev_b32_e32 v2, 10, v235
	ds_write_b64 v230, v[14:15] offset:4608
	v_cvt_pk_bf16_f32 v14, v58, v59
	v_cvt_pk_bf16_f32 v15, v60, v61
	v_cvt_pk_bf16_f32 v7, v12, v13
	ds_write_b64 v225, v[6:7] offset:7168
	v_and_or_b32 v6, v2, s0, v203
	ds_write_b64 v229, v[14:15] offset:5120
	v_cvt_pk_bf16_f32 v14, v30, v31
	v_cvt_pk_bf16_f32 v15, v32, v33
	v_or_b32_e32 v7, 0x2000, v6
	ds_write_b64 v228, v[14:15] offset:5632
	v_cvt_pk_bf16_f32 v14, v34, v35
	v_cvt_pk_bf16_f32 v15, v36, v37
	buffer_load_dwordx4 v[2:5], v6, s[4:7], 0 offen nt
	buffer_load_dwordx4 v[10:13], v7, s[4:7], 0 offen nt
	v_or_b32_e32 v7, 0x4000, v6
	ds_write_b64 v227, v[14:15] offset:6144
	buffer_load_dwordx4 v[14:17], v7, s[4:7], 0 offen nt
	v_or_b32_e32 v7, 0x6000, v6
	v_cvt_pk_bf16_f32 v38, v38, v39
	v_cvt_pk_bf16_f32 v39, v40, v41
	buffer_load_dwordx4 v[22:25], v7, s[4:7], 0 offen nt
	v_or_b32_e32 v7, 0x8000, v6
	ds_write_b64 v211, v[38:39] offset:512
	v_cvt_pk_bf16_f32 v38, v42, v43
	v_cvt_pk_bf16_f32 v39, v44, v45
	buffer_load_dwordx4 v[30:33], v7, s[4:7], 0 offen nt
	v_or_b32_e32 v7, 0xa000, v6
	ds_write_b64 v210, v[38:39] offset:1024
	buffer_load_dwordx4 v[38:41], v7, s[4:7], 0 offen nt
	v_or_b32_e32 v7, 0xc000, v6
	buffer_load_dwordx4 v[46:49], v7, s[4:7], 0 offen nt
	v_or_b32_e32 v7, 0xe000, v6
	v_cvt_pk_bf16_f32 v62, v62, v63
	v_cvt_pk_bf16_f32 v63, v64, v65
	buffer_load_dwordx4 v[54:57], v7, s[4:7], 0 offen nt
	v_or_b32_e32 v7, 0x10000, v6
	ds_write_b64 v212, v[62:63]
	buffer_load_dwordx4 v[62:65], v7, s[4:7], 0 offen nt
	v_or_b32_e32 v7, 0x12000, v6
	s_waitcnt lgkmcnt(14)
	v_mfma_f32_16x16x32_bf16 v[66:69], v[74:77], v[82:85], v[66:69]
	v_mfma_f32_16x16x32_bf16 v[74:77], v[78:81], v[82:85], v[70:73]
	s_nop 2
	buffer_load_dwordx4 v[70:73], v7, s[4:7], 0 offen nt
	v_or_b32_e32 v7, 0x14000, v6
	buffer_load_dwordx4 v[78:81], v7, s[4:7], 0 offen nt
	v_or_b32_e32 v7, 0x16000, v6
	buffer_load_dwordx4 v[86:89], v7, s[4:7], 0 offen nt
	v_or_b32_e32 v7, 0x18000, v6
	buffer_load_dwordx4 v[94:97], v7, s[4:7], 0 offen nt
	v_or_b32_e32 v7, 0x1a000, v6
	buffer_load_dwordx4 v[146:149], v7, s[4:7], 0 offen nt
	v_or_b32_e32 v7, 0x1c000, v6
	v_or_b32_e32 v6, 0x1e000, v6
	buffer_load_dwordx4 v[150:153], v7, s[4:7], 0 offen nt
	buffer_load_dwordx4 v[154:157], v6, s[4:7], 0 offen nt
	v_add_u32_e32 v6, 8, v232
	v_and_b32_e32 v50, 56, v6
	v_lshl_or_b32 v6, v50, 10, v198
	ds_read_b128 v[6:9], v6
	v_lshl_or_b32 v18, v50, 8, v204
	ds_read_b128 v[18:21], v18
	ds_read_b128 v[26:29], v223
	v_or_b32_e32 v34, 1, v50
	s_movk_i32 s24, 0x1000
	s_waitcnt lgkmcnt(0)
	v_mfma_f32_16x16x32_bf16 v[18:21], v[18:21], v[26:29], v[74:77]
	v_add_u32_e32 v234, 5, v200
	v_mfma_f32_16x16x32_bf16 v[6:9], v[6:9], v[26:29], v[66:69]
	v_lshl_or_b32 v26, v34, 10, v198
	ds_read_b128 v[26:29], v26
	v_lshl_or_b32 v34, v34, 8, v204
	ds_read_b128 v[34:37], v34
	ds_read_b128 v[42:45], v222
	s_waitcnt lgkmcnt(0)
	v_mfma_f32_16x16x32_bf16 v[18:21], v[34:37], v[42:45], v[18:21]
	v_or_b32_e32 v34, 2, v50
	v_mfma_f32_16x16x32_bf16 v[6:9], v[26:29], v[42:45], v[6:9]
	v_lshl_or_b32 v26, v34, 10, v198
	ds_read_b128 v[26:29], v26
	v_lshl_or_b32 v34, v34, 8, v204
	ds_read_b128 v[34:37], v34
	ds_read_b128 v[42:45], v221
	s_waitcnt lgkmcnt(0)
	v_mfma_f32_16x16x32_bf16 v[18:21], v[34:37], v[42:45], v[18:21]
	v_or_b32_e32 v34, 3, v50
	v_mfma_f32_16x16x32_bf16 v[6:9], v[26:29], v[42:45], v[6:9]
	v_lshl_or_b32 v26, v34, 10, v198
	ds_read_b128 v[26:29], v26
	v_lshl_or_b32 v34, v34, 8, v204
	ds_read_b128 v[34:37], v34
	ds_read_b128 v[42:45], v219
	s_waitcnt lgkmcnt(0)
	v_mfma_f32_16x16x32_bf16 v[18:21], v[34:37], v[42:45], v[18:21]
	v_or_b32_e32 v34, 4, v50
	v_mfma_f32_16x16x32_bf16 v[6:9], v[26:29], v[42:45], v[6:9]
	v_lshl_or_b32 v26, v34, 10, v198
	ds_read_b128 v[26:29], v26
	v_lshl_or_b32 v34, v34, 8, v204
	ds_read_b128 v[34:37], v34
	ds_read_b128 v[42:45], v218
	s_waitcnt lgkmcnt(0)
	v_mfma_f32_16x16x32_bf16 v[18:21], v[34:37], v[42:45], v[18:21]
	v_or_b32_e32 v34, 5, v50
	v_mfma_f32_16x16x32_bf16 v[6:9], v[26:29], v[42:45], v[6:9]
	v_lshl_or_b32 v26, v34, 10, v198
	ds_read_b128 v[26:29], v26
	v_lshl_or_b32 v34, v34, 8, v204
	ds_read_b128 v[34:37], v34
	ds_read_b128 v[42:45], v217
	s_waitcnt lgkmcnt(0)
	v_mfma_f32_16x16x32_bf16 v[18:21], v[34:37], v[42:45], v[18:21]
	v_or_b32_e32 v34, 6, v50
	v_mfma_f32_16x16x32_bf16 v[6:9], v[26:29], v[42:45], v[6:9]
	v_lshl_or_b32 v26, v34, 10, v198
	ds_read_b128 v[26:29], v26
	v_lshl_or_b32 v34, v34, 8, v204
	ds_read_b128 v[34:37], v34
	ds_read_b128 v[42:45], v216
	s_waitcnt lgkmcnt(0)
	v_mfma_f32_16x16x32_bf16 v[18:21], v[34:37], v[42:45], v[18:21]
	v_or_b32_e32 v34, 7, v50
	v_mfma_f32_16x16x32_bf16 v[6:9], v[26:29], v[42:45], v[6:9]
	v_lshl_or_b32 v26, v34, 10, v198
	ds_read_b128 v[26:29], v26
	v_lshl_or_b32 v34, v34, 8, v204
	ds_read_b128 v[34:37], v34
	ds_read_b128 v[42:45], v213
	s_waitcnt lgkmcnt(0)
	v_mfma_f32_16x16x32_bf16 v[162:165], v[26:29], v[42:45], v[6:9]
	s_waitcnt vmcnt(31)
	s_nop 1
	v_cvt_pk_bf16_f32 v6, v102, v103
	v_cvt_pk_bf16_f32 v7, v104, v105
	ds_write_b64 v212, v[6:7]
	s_waitcnt vmcnt(30)
	v_cvt_pk_bf16_f32 v6, v98, v99
	v_cvt_pk_bf16_f32 v7, v100, v101
	ds_write_b64 v211, v[6:7] offset:512
	s_waitcnt vmcnt(29)
	v_cvt_pk_bf16_f32 v6, v110, v111
	v_cvt_pk_bf16_f32 v7, v112, v113
	ds_write_b64 v210, v[6:7] offset:1024
	s_waitcnt vmcnt(28)
	v_cvt_pk_bf16_f32 v6, v106, v107
	v_cvt_pk_bf16_f32 v7, v108, v109
	ds_write_b64 v209, v[6:7] offset:1536
	s_waitcnt vmcnt(27)
	v_cvt_pk_bf16_f32 v6, v118, v119
	v_cvt_pk_bf16_f32 v7, v120, v121
	ds_write_b64 v208, v[6:7] offset:2048
	s_waitcnt vmcnt(26)
	v_cvt_pk_bf16_f32 v6, v114, v115
	v_cvt_pk_bf16_f32 v7, v116, v117
	ds_write_b64 v207, v[6:7] offset:2560
	s_waitcnt vmcnt(25)
	v_cvt_pk_bf16_f32 v6, v126, v127
	v_cvt_pk_bf16_f32 v7, v128, v129
	ds_write_b64 v206, v[6:7] offset:3072
	s_waitcnt vmcnt(24)
	v_cvt_pk_bf16_f32 v6, v122, v123
	v_cvt_pk_bf16_f32 v7, v124, v125
	ds_write_b64 v205, v[6:7] offset:3584
	s_waitcnt vmcnt(23)
	v_cvt_pk_bf16_f32 v6, v134, v135
	v_cvt_pk_bf16_f32 v7, v136, v137
	ds_write_b64 v231, v[6:7] offset:4096
	s_waitcnt vmcnt(22)
	v_cvt_pk_bf16_f32 v6, v130, v131
	v_cvt_pk_bf16_f32 v7, v132, v133
	ds_write_b64 v230, v[6:7] offset:4608
	s_waitcnt vmcnt(21)
	v_cvt_pk_bf16_f32 v6, v142, v143
	v_cvt_pk_bf16_f32 v7, v144, v145
	ds_write_b64 v229, v[6:7] offset:5120
	s_waitcnt vmcnt(20)
	v_cvt_pk_bf16_f32 v6, v138, v139
	v_cvt_pk_bf16_f32 v7, v140, v141
	ds_write_b64 v228, v[6:7] offset:5632
	s_waitcnt vmcnt(19)
	v_cvt_pk_bf16_f32 v6, v170, v171
	v_cvt_pk_bf16_f32 v7, v172, v173
	ds_write_b64 v227, v[6:7] offset:6144
	s_waitcnt vmcnt(18)
	v_cvt_pk_bf16_f32 v6, v158, v159
	v_mov_b32_e32 v106, 0x1000
	v_cvt_pk_bf16_f32 v7, v160, v161
	ds_write_b64 v226, v[6:7] offset:6656
	s_waitcnt vmcnt(17)
	v_cvt_pk_bf16_f32 v6, v190, v191
	v_bitop3_b32 v107, v233, s19, v106 bitop3:0xde
	v_mfma_f32_16x16x32_bf16 v[166:169], v[34:37], v[42:45], v[18:21]
	v_cvt_pk_bf16_f32 v7, v192, v193
	ds_write_b64 v225, v[6:7] offset:7168
	s_waitcnt vmcnt(16)
	v_cvt_pk_bf16_f32 v6, v186, v187
	v_bitop3_b32 v26, v233, s17, v106 bitop3:0xde
	v_bitop3_b32 v34, v233, s11, v106 bitop3:0xde
	v_bitop3_b32 v18, v233, s16, v106 bitop3:0xde
	v_bitop3_b32 v42, v233, s13, v106 bitop3:0xde
	v_bitop3_b32 v50, v233, s10, v106 bitop3:0xde
	v_bitop3_b32 v58, v233, s12, v106 bitop3:0xde
	v_bitop3_b32 v66, v233, s1, v106 bitop3:0xde
	v_bitop3_b32 v74, v233, s18, v106 bitop3:0xde
	v_bitop3_b32 v82, v233, s23, v106 bitop3:0xde
	v_bitop3_b32 v90, v233, s22, v106 bitop3:0xde
	v_bitop3_b32 v98, v233, s21, v106 bitop3:0xde
	v_bitop3_b32 v102, v233, s20, v106 bitop3:0xde
	buffer_load_dwordx4 v[110:113], v107, s[4:7], 0 offen nt
	v_bitop3_b32 v107, v233, s15, v106 bitop3:0xde
	v_bitop3_b32 v106, v233, s14, v106 bitop3:0xde
	v_cvt_pk_bf16_f32 v7, v188, v189
	ds_write_b64 v224, v[6:7] offset:7680
	v_bitop3_b32 v6, v203, s24, v196 bitop3:0x36
	buffer_load_dwordx4 v[42:45], v42, s[4:7], 0 offen nt
	s_nop 0
	buffer_load_dwordx4 v[50:53], v50, s[4:7], 0 offen nt
	s_nop 0
	buffer_load_dwordx4 v[58:61], v58, s[4:7], 0 offen nt
	s_nop 0
	buffer_load_dwordx4 v[66:69], v66, s[4:7], 0 offen nt
	s_nop 0
	buffer_load_dwordx4 v[74:77], v74, s[4:7], 0 offen nt
	s_nop 0
	buffer_load_dwordx4 v[82:85], v82, s[4:7], 0 offen nt
	s_nop 0
	buffer_load_dwordx4 v[90:93], v90, s[4:7], 0 offen nt
	s_nop 0
	buffer_load_dwordx4 v[98:101], v98, s[4:7], 0 offen nt
	s_nop 0
	buffer_load_dwordx4 v[102:105], v102, s[4:7], 0 offen nt
	s_nop 0
	buffer_load_dwordx4 v[126:129], v106, s[4:7], 0 offen nt
	buffer_load_dwordx4 v[118:121], v107, s[4:7], 0 offen nt
	s_nop 0
	buffer_load_dwordx4 v[6:9], v6, s[4:7], 0 offen nt
	s_nop 0
	buffer_load_dwordx4 v[18:21], v18, s[4:7], 0 offen nt
	s_nop 0
	buffer_load_dwordx4 v[26:29], v26, s[4:7], 0 offen nt
	s_nop 0
	buffer_load_dwordx4 v[34:37], v34, s[4:7], 0 offen nt
	v_add_u32_e32 v106, 16, v232
	v_and_b32_e32 v138, 56, v106
	v_lshl_or_b32 v106, v138, 10, v198
	ds_read_b128 v[106:109], v106
	v_lshl_or_b32 v114, v138, 8, v204
	ds_read_b128 v[114:117], v114
	ds_read_b128 v[122:125], v223
	v_or_b32_e32 v130, 1, v138
	s_waitcnt vmcnt(31)
	v_cvt_pk_bf16_f32 v2, v2, v3
	s_waitcnt lgkmcnt(0)
	v_mfma_f32_16x16x32_bf16 v[114:117], v[114:117], v[122:125], v[166:169]
	v_cvt_pk_bf16_f32 v3, v4, v5
	v_mfma_f32_16x16x32_bf16 v[106:109], v[106:109], v[122:125], v[162:165]
	v_lshl_or_b32 v122, v130, 10, v198
	ds_read_b128 v[122:125], v122
	v_lshl_or_b32 v130, v130, 8, v204
	ds_read_b128 v[130:133], v130
	ds_read_b128 v[134:137], v222
	s_waitcnt lgkmcnt(0)
	v_mfma_f32_16x16x32_bf16 v[114:117], v[130:133], v[134:137], v[114:117]
	v_or_b32_e32 v130, 2, v138
	v_mfma_f32_16x16x32_bf16 v[106:109], v[122:125], v[134:137], v[106:109]
	v_lshl_or_b32 v122, v130, 10, v198
	ds_read_b128 v[122:125], v122
	v_lshl_or_b32 v130, v130, 8, v204
	ds_read_b128 v[130:133], v130
	ds_read_b128 v[134:137], v221
	s_waitcnt lgkmcnt(0)
	v_mfma_f32_16x16x32_bf16 v[114:117], v[130:133], v[134:137], v[114:117]
	v_or_b32_e32 v130, 3, v138
	v_mfma_f32_16x16x32_bf16 v[106:109], v[122:125], v[134:137], v[106:109]
	v_lshl_or_b32 v122, v130, 10, v198
	ds_read_b128 v[122:125], v122
	v_lshl_or_b32 v130, v130, 8, v204
	ds_read_b128 v[130:133], v130
	ds_read_b128 v[134:137], v219
	s_waitcnt lgkmcnt(0)
	v_mfma_f32_16x16x32_bf16 v[114:117], v[130:133], v[134:137], v[114:117]
	v_or_b32_e32 v130, 4, v138
	v_mfma_f32_16x16x32_bf16 v[106:109], v[122:125], v[134:137], v[106:109]
	v_lshl_or_b32 v122, v130, 10, v198
	ds_read_b128 v[122:125], v122
	v_lshl_or_b32 v130, v130, 8, v204
	ds_read_b128 v[130:133], v130
	ds_read_b128 v[134:137], v218
	s_waitcnt lgkmcnt(0)
	v_mfma_f32_16x16x32_bf16 v[114:117], v[130:133], v[134:137], v[114:117]
	v_or_b32_e32 v130, 5, v138
	v_mfma_f32_16x16x32_bf16 v[106:109], v[122:125], v[134:137], v[106:109]
	v_lshl_or_b32 v122, v130, 10, v198
	ds_read_b128 v[122:125], v122
	v_lshl_or_b32 v130, v130, 8, v204
	ds_read_b128 v[130:133], v130
	ds_read_b128 v[134:137], v217
	s_waitcnt lgkmcnt(0)
	v_mfma_f32_16x16x32_bf16 v[114:117], v[130:133], v[134:137], v[114:117]
	v_or_b32_e32 v130, 6, v138
	v_mfma_f32_16x16x32_bf16 v[106:109], v[122:125], v[134:137], v[106:109]
	v_lshl_or_b32 v122, v130, 10, v198
	ds_read_b128 v[122:125], v122
	v_lshl_or_b32 v130, v130, 8, v204
	ds_read_b128 v[130:133], v130
	ds_read_b128 v[134:137], v216
	s_waitcnt lgkmcnt(0)
	v_mfma_f32_16x16x32_bf16 v[114:117], v[130:133], v[134:137], v[114:117]
	v_or_b32_e32 v130, 7, v138
	v_mfma_f32_16x16x32_bf16 v[106:109], v[122:125], v[134:137], v[106:109]
	v_lshl_or_b32 v122, v130, 10, v198
	v_lshl_or_b32 v130, v130, 8, v204
	ds_read_b128 v[122:125], v122
	ds_read_b128 v[134:137], v130
	ds_read_b128 v[138:141], v213
	ds_write_b64 v212, v[2:3]
	s_waitcnt vmcnt(30)
	v_cvt_pk_bf16_f32 v2, v10, v11
	v_cvt_pk_bf16_f32 v3, v12, v13
	ds_write_b64 v211, v[2:3] offset:512
	s_waitcnt vmcnt(29)
	v_cvt_pk_bf16_f32 v2, v14, v15
	v_cvt_pk_bf16_f32 v3, v16, v17
	ds_write_b64 v210, v[2:3] offset:1024
	s_waitcnt vmcnt(28)
	v_cvt_pk_bf16_f32 v2, v22, v23
	v_cvt_pk_bf16_f32 v3, v24, v25
	ds_write_b64 v209, v[2:3] offset:1536
	s_waitcnt vmcnt(27)
	v_cvt_pk_bf16_f32 v2, v30, v31
	v_cvt_pk_bf16_f32 v3, v32, v33
	ds_write_b64 v208, v[2:3] offset:2048
	s_waitcnt vmcnt(26)
	v_cvt_pk_bf16_f32 v2, v38, v39
	v_cvt_pk_bf16_f32 v3, v40, v41
	ds_write_b64 v207, v[2:3] offset:2560
	s_waitcnt vmcnt(25)
	v_cvt_pk_bf16_f32 v2, v46, v47
	v_cvt_pk_bf16_f32 v3, v48, v49
	ds_write_b64 v206, v[2:3] offset:3072
	s_waitcnt vmcnt(24)
	v_cvt_pk_bf16_f32 v2, v54, v55
	v_cvt_pk_bf16_f32 v3, v56, v57
	ds_write_b64 v205, v[2:3] offset:3584
	s_waitcnt vmcnt(23)
	v_cvt_pk_bf16_f32 v2, v62, v63
	v_cvt_pk_bf16_f32 v3, v64, v65
	ds_write_b64 v231, v[2:3] offset:4096
	s_waitcnt vmcnt(22)
	v_cvt_pk_bf16_f32 v2, v70, v71
	v_cvt_pk_bf16_f32 v3, v72, v73
	ds_write_b64 v230, v[2:3] offset:4608
	s_waitcnt vmcnt(21)
	v_cvt_pk_bf16_f32 v2, v78, v79
	v_cvt_pk_bf16_f32 v3, v80, v81
	ds_write_b64 v229, v[2:3] offset:5120
	s_waitcnt vmcnt(20)
	v_cvt_pk_bf16_f32 v2, v86, v87
	v_cvt_pk_bf16_f32 v3, v88, v89
	ds_write_b64 v228, v[2:3] offset:5632
	s_waitcnt vmcnt(19)
	v_cvt_pk_bf16_f32 v2, v94, v95
	v_cvt_pk_bf16_f32 v3, v96, v97
	ds_write_b64 v227, v[2:3] offset:6144
	s_waitcnt vmcnt(18)
	v_cvt_pk_bf16_f32 v2, v146, v147
	v_cvt_pk_bf16_f32 v3, v148, v149
	ds_write_b64 v226, v[2:3] offset:6656
	s_waitcnt vmcnt(17)
	v_cvt_pk_bf16_f32 v2, v150, v151
	v_cvt_pk_bf16_f32 v3, v152, v153
	ds_write_b64 v225, v[2:3] offset:7168
	s_waitcnt vmcnt(16)
	v_cvt_pk_bf16_f32 v2, v154, v155
	v_cvt_pk_bf16_f32 v3, v156, v157
	ds_write_b64 v224, v[2:3] offset:7680
	v_lshlrev_b32_e32 v2, 10, v234
	s_waitcnt lgkmcnt(14)
	v_mfma_f32_16x16x32_bf16 v[130:133], v[122:125], v[138:141], v[106:109]
	v_and_or_b32 v122, v2, s0, v203
	buffer_load_dwordx4 v[2:5], v122, s[4:7], 0 offen nt
	v_or_b32_e32 v10, 0x2000, v122
	v_mfma_f32_16x16x32_bf16 v[134:137], v[134:137], v[138:141], v[114:117]
	v_or_b32_e32 v14, 0x4000, v122
	v_or_b32_e32 v22, 0x6000, v122
	v_or_b32_e32 v30, 0x8000, v122
	v_or_b32_e32 v38, 0xa000, v122
	v_or_b32_e32 v46, 0xc000, v122
	v_or_b32_e32 v54, 0xe000, v122
	v_or_b32_e32 v62, 0x10000, v122
	v_or_b32_e32 v70, 0x12000, v122
	v_or_b32_e32 v78, 0x14000, v122
	v_or_b32_e32 v86, 0x16000, v122
	v_or_b32_e32 v94, 0x18000, v122
	v_or_b32_e32 v106, 0x1a000, v122
	v_or_b32_e32 v114, 0x1c000, v122
	v_or_b32_e32 v122, 0x1e000, v122
	buffer_load_dwordx4 v[54:57], v54, s[4:7], 0 offen nt
	s_nop 0
	buffer_load_dwordx4 v[62:65], v62, s[4:7], 0 offen nt
	s_nop 0
	buffer_load_dwordx4 v[70:73], v70, s[4:7], 0 offen nt
	s_nop 0
	buffer_load_dwordx4 v[78:81], v78, s[4:7], 0 offen nt
	s_nop 0
	buffer_load_dwordx4 v[86:89], v86, s[4:7], 0 offen nt
	s_nop 0
	buffer_load_dwordx4 v[94:97], v94, s[4:7], 0 offen nt
	s_nop 0
	buffer_load_dwordx4 v[106:109], v106, s[4:7], 0 offen nt
	s_nop 0
	buffer_load_dwordx4 v[114:117], v114, s[4:7], 0 offen nt
	s_nop 0
	buffer_load_dwordx4 v[122:125], v122, s[4:7], 0 offen nt
	s_nop 0
	buffer_load_dwordx4 v[10:13], v10, s[4:7], 0 offen nt
	s_nop 0
	buffer_load_dwordx4 v[14:17], v14, s[4:7], 0 offen nt
	s_nop 0
	buffer_load_dwordx4 v[22:25], v22, s[4:7], 0 offen nt
	s_nop 0
	buffer_load_dwordx4 v[30:33], v30, s[4:7], 0 offen nt
	s_nop 0
	buffer_load_dwordx4 v[38:41], v38, s[4:7], 0 offen nt
	s_nop 0
	buffer_load_dwordx4 v[46:49], v46, s[4:7], 0 offen nt
	v_lshlrev_b32_e32 v138, 3, v235
	v_and_b32_e32 v150, 56, v138
	v_lshl_or_b32 v138, v150, 10, v198
	ds_read_b128 v[138:141], v138
	v_lshl_or_b32 v142, v150, 8, v204
	ds_read_b128 v[142:145], v142
	ds_read_b128 v[146:149], v223
	s_waitcnt vmcnt(19)
	v_cvt_pk_bf16_f32 v6, v6, v7
	v_cvt_pk_bf16_f32 v7, v8, v9
	s_waitcnt lgkmcnt(0)
	v_mfma_f32_16x16x32_bf16 v[134:137], v[142:145], v[146:149], v[134:137]
	v_or_b32_e32 v142, 1, v150
	v_mfma_f32_16x16x32_bf16 v[130:133], v[138:141], v[146:149], v[130:133]
	v_lshl_or_b32 v138, v142, 10, v198
	ds_read_b128 v[138:141], v138
	v_lshl_or_b32 v142, v142, 8, v204
	ds_read_b128 v[142:145], v142
	ds_read_b128 v[146:149], v222
	s_waitcnt lgkmcnt(0)
	v_mfma_f32_16x16x32_bf16 v[134:137], v[142:145], v[146:149], v[134:137]
	v_or_b32_e32 v142, 2, v150
	v_mfma_f32_16x16x32_bf16 v[130:133], v[138:141], v[146:149], v[130:133]
	v_lshl_or_b32 v138, v142, 10, v198
	ds_read_b128 v[138:141], v138
	v_lshl_or_b32 v142, v142, 8, v204
	ds_read_b128 v[142:145], v142
	ds_read_b128 v[146:149], v221
	s_waitcnt lgkmcnt(0)
	v_mfma_f32_16x16x32_bf16 v[134:137], v[142:145], v[146:149], v[134:137]
	v_or_b32_e32 v142, 3, v150
	v_mfma_f32_16x16x32_bf16 v[130:133], v[138:141], v[146:149], v[130:133]
	v_lshl_or_b32 v138, v142, 10, v198
	ds_read_b128 v[138:141], v138
	v_lshl_or_b32 v142, v142, 8, v204
	ds_read_b128 v[142:145], v142
	ds_read_b128 v[146:149], v219
	s_waitcnt lgkmcnt(0)
	v_mfma_f32_16x16x32_bf16 v[134:137], v[142:145], v[146:149], v[134:137]
	v_or_b32_e32 v142, 4, v150
	v_mfma_f32_16x16x32_bf16 v[130:133], v[138:141], v[146:149], v[130:133]
	v_lshl_or_b32 v138, v142, 10, v198
	ds_read_b128 v[138:141], v138
	v_lshl_or_b32 v142, v142, 8, v204
	ds_read_b128 v[142:145], v142
	ds_read_b128 v[146:149], v218
	s_waitcnt lgkmcnt(0)
	v_mfma_f32_16x16x32_bf16 v[134:137], v[142:145], v[146:149], v[134:137]
	v_or_b32_e32 v142, 5, v150
	v_mfma_f32_16x16x32_bf16 v[130:133], v[138:141], v[146:149], v[130:133]
	v_lshl_or_b32 v138, v142, 10, v198
	ds_read_b128 v[138:141], v138
	v_lshl_or_b32 v142, v142, 8, v204
	ds_read_b128 v[142:145], v142
	ds_read_b128 v[146:149], v217
	s_waitcnt lgkmcnt(0)
	v_mfma_f32_16x16x32_bf16 v[134:137], v[142:145], v[146:149], v[134:137]
	v_or_b32_e32 v142, 6, v150
	v_mfma_f32_16x16x32_bf16 v[130:133], v[138:141], v[146:149], v[130:133]
	v_lshl_or_b32 v138, v142, 10, v198
	ds_read_b128 v[138:141], v138
	v_lshl_or_b32 v142, v142, 8, v204
	ds_read_b128 v[142:145], v142
	ds_read_b128 v[146:149], v216
	s_waitcnt lgkmcnt(0)
	v_mfma_f32_16x16x32_bf16 v[134:137], v[142:145], v[146:149], v[134:137]
	v_or_b32_e32 v142, 7, v150
	v_mfma_f32_16x16x32_bf16 v[130:133], v[138:141], v[146:149], v[130:133]
	v_lshl_or_b32 v138, v142, 10, v198
	v_lshl_or_b32 v142, v142, 8, v204
	ds_read_b128 v[138:141], v138
	ds_read_b128 v[142:145], v142
	ds_read_b128 v[146:149], v213
	ds_write_b64 v212, v[6:7]
	s_waitcnt vmcnt(18)
	v_cvt_pk_bf16_f32 v6, v18, v19
	v_cvt_pk_bf16_f32 v7, v20, v21
	ds_write_b64 v211, v[6:7] offset:512
	s_waitcnt vmcnt(17)
	v_cvt_pk_bf16_f32 v6, v26, v27
	v_cvt_pk_bf16_f32 v7, v28, v29
	ds_write_b64 v210, v[6:7] offset:1024
	s_waitcnt vmcnt(16)
	v_cvt_pk_bf16_f32 v6, v34, v35
	v_cvt_pk_bf16_f32 v7, v36, v37
	ds_write_b64 v209, v[6:7] offset:1536
	v_cvt_pk_bf16_f32 v6, v42, v43
	v_cvt_pk_bf16_f32 v7, v44, v45
	ds_write_b64 v208, v[6:7] offset:2048
	v_cvt_pk_bf16_f32 v6, v50, v51
	v_cvt_pk_bf16_f32 v7, v52, v53
	ds_write_b64 v207, v[6:7] offset:2560
	v_cvt_pk_bf16_f32 v6, v58, v59
	v_cvt_pk_bf16_f32 v7, v60, v61
	ds_write_b64 v206, v[6:7] offset:3072
	v_cvt_pk_bf16_f32 v6, v66, v67
	v_cvt_pk_bf16_f32 v7, v68, v69
	ds_write_b64 v205, v[6:7] offset:3584
	v_cvt_pk_bf16_f32 v6, v74, v75
	v_cvt_pk_bf16_f32 v7, v76, v77
	ds_write_b64 v231, v[6:7] offset:4096
	v_cvt_pk_bf16_f32 v6, v82, v83
	v_cvt_pk_bf16_f32 v7, v84, v85
	ds_write_b64 v230, v[6:7] offset:4608
	v_cvt_pk_bf16_f32 v6, v90, v91
	v_cvt_pk_bf16_f32 v7, v92, v93
	ds_write_b64 v229, v[6:7] offset:5120
	v_cvt_pk_bf16_f32 v6, v98, v99
	v_cvt_pk_bf16_f32 v7, v100, v101
	ds_write_b64 v228, v[6:7] offset:5632
	v_cvt_pk_bf16_f32 v6, v102, v103
	v_cvt_pk_bf16_f32 v7, v104, v105
	ds_write_b64 v227, v[6:7] offset:6144
	v_cvt_pk_bf16_f32 v6, v110, v111
	v_cvt_pk_bf16_f32 v7, v112, v113
	ds_write_b64 v226, v[6:7] offset:6656
	v_cvt_pk_bf16_f32 v6, v118, v119
	v_cvt_pk_bf16_f32 v7, v120, v121
	ds_write_b64 v225, v[6:7] offset:7168
	v_cvt_pk_bf16_f32 v6, v126, v127
	v_cvt_pk_bf16_f32 v7, v128, v129
	ds_write_b64 v224, v[6:7] offset:7680
	v_add_u32_e32 v6, 0x1800, v196
	v_and_or_b32 v126, v6, s0, v203
	buffer_load_dwordx4 v[6:9], v126, s[4:7], 0 offen nt
	v_or_b32_e32 v18, 0x2000, v126
	v_or_b32_e32 v26, 0x4000, v126
	v_or_b32_e32 v34, 0x6000, v126
	v_or_b32_e32 v42, 0x8000, v126
	v_or_b32_e32 v50, 0xa000, v126
	v_or_b32_e32 v58, 0xc000, v126
	v_or_b32_e32 v66, 0xe000, v126
	v_or_b32_e32 v74, 0x10000, v126
	v_or_b32_e32 v82, 0x12000, v126
	v_or_b32_e32 v90, 0x14000, v126
	v_or_b32_e32 v98, 0x16000, v126
	v_or_b32_e32 v102, 0x18000, v126
	v_or_b32_e32 v110, 0x1a000, v126
	v_or_b32_e32 v118, 0x1c000, v126
	v_or_b32_e32 v126, 0x1e000, v126
	buffer_load_dwordx4 v[50:53], v50, s[4:7], 0 offen nt
	s_waitcnt lgkmcnt(14)
	v_mfma_f32_16x16x32_bf16 v[130:133], v[138:141], v[146:149], v[130:133]
	buffer_load_dwordx4 v[58:61], v58, s[4:7], 0 offen nt
	s_nop 0
	buffer_load_dwordx4 v[66:69], v66, s[4:7], 0 offen nt
	v_mfma_f32_16x16x32_bf16 v[134:137], v[142:145], v[146:149], v[134:137]
	buffer_load_dwordx4 v[74:77], v74, s[4:7], 0 offen nt
	v_add_u32_e32 v142, 7, v200
	buffer_load_dwordx4 v[82:85], v82, s[4:7], 0 offen nt
	s_nop 0
	buffer_load_dwordx4 v[90:93], v90, s[4:7], 0 offen nt
	s_nop 0
	buffer_load_dwordx4 v[98:101], v98, s[4:7], 0 offen nt
	s_nop 0
	buffer_load_dwordx4 v[102:105], v102, s[4:7], 0 offen nt
	s_nop 0
	buffer_load_dwordx4 v[110:113], v110, s[4:7], 0 offen nt
	s_nop 0
	buffer_load_dwordx4 v[118:121], v118, s[4:7], 0 offen nt
	s_nop 0
	buffer_load_dwordx4 v[126:129], v126, s[4:7], 0 offen nt
	s_nop 0
	buffer_load_dwordx4 v[18:21], v18, s[4:7], 0 offen nt
	s_nop 0
	buffer_load_dwordx4 v[26:29], v26, s[4:7], 0 offen nt
	s_nop 0
	buffer_load_dwordx4 v[34:37], v34, s[4:7], 0 offen nt
	s_nop 0
	buffer_load_dwordx4 v[42:45], v42, s[4:7], 0 offen nt
	v_xor_b32_e32 v143, 32, v232
	v_lshl_or_b32 v138, v143, 10, v198
	ds_read_b128 v[138:141], v138
	v_lshl_or_b32 v143, v143, 8, v204
	ds_read_b128 v[144:147], v143
	ds_read_b128 v[148:151], v223
	v_bitop3_b32 v143, v232, 1, 32 bitop3:0xde
	s_waitcnt vmcnt(31)
	v_cvt_pk_bf16_f32 v2, v2, v3
	s_waitcnt lgkmcnt(0)
	v_mfma_f32_16x16x32_bf16 v[134:137], v[144:147], v[148:151], v[134:137]
	v_cvt_pk_bf16_f32 v3, v4, v5
	v_mfma_f32_16x16x32_bf16 v[130:133], v[138:141], v[148:151], v[130:133]
	v_lshl_or_b32 v138, v143, 10, v198
	ds_read_b128 v[138:141], v138
	v_lshl_or_b32 v143, v143, 8, v204
	ds_read_b128 v[144:147], v143
	ds_read_b128 v[148:151], v222
	v_bitop3_b32 v143, v232, 2, 32 bitop3:0xde
	s_waitcnt lgkmcnt(0)
	v_mfma_f32_16x16x32_bf16 v[134:137], v[144:147], v[148:151], v[134:137]
	v_mfma_f32_16x16x32_bf16 v[130:133], v[138:141], v[148:151], v[130:133]
	v_lshl_or_b32 v138, v143, 10, v198
	ds_read_b128 v[138:141], v138
	v_lshl_or_b32 v143, v143, 8, v204
	ds_read_b128 v[144:147], v143
	ds_read_b128 v[148:151], v221
	v_bitop3_b32 v143, v232, 3, 32 bitop3:0xde
	s_waitcnt lgkmcnt(0)
	v_mfma_f32_16x16x32_bf16 v[130:133], v[138:141], v[148:151], v[130:133]
	v_lshl_or_b32 v138, v143, 10, v198
	ds_read_b128 v[138:141], v138
	v_lshl_or_b32 v143, v143, 8, v204
	v_mfma_f32_16x16x32_bf16 v[134:137], v[144:147], v[148:151], v[134:137]
	ds_read_b128 v[144:147], v143
	ds_read_b128 v[148:151], v219
	v_bitop3_b32 v143, v232, 4, 32 bitop3:0xde
	s_waitcnt lgkmcnt(0)
	v_mfma_f32_16x16x32_bf16 v[130:133], v[138:141], v[148:151], v[130:133]
	v_lshl_or_b32 v138, v143, 10, v198
	ds_read_b128 v[138:141], v138
	v_lshl_or_b32 v143, v143, 8, v204
	v_mfma_f32_16x16x32_bf16 v[134:137], v[144:147], v[148:151], v[134:137]
	ds_read_b128 v[144:147], v143
	ds_read_b128 v[148:151], v218
	v_bitop3_b32 v143, v232, 5, 32 bitop3:0xde
	s_waitcnt lgkmcnt(0)
	v_mfma_f32_16x16x32_bf16 v[130:133], v[138:141], v[148:151], v[130:133]
	v_lshl_or_b32 v138, v143, 10, v198
	ds_read_b128 v[138:141], v138
	v_lshl_or_b32 v143, v143, 8, v204
	v_mfma_f32_16x16x32_bf16 v[134:137], v[144:147], v[148:151], v[134:137]
	ds_read_b128 v[144:147], v143
	ds_read_b128 v[148:151], v217
	v_bitop3_b32 v143, v232, 6, 32 bitop3:0xde
	s_waitcnt lgkmcnt(0)
	v_mfma_f32_16x16x32_bf16 v[130:133], v[138:141], v[148:151], v[130:133]
	v_lshl_or_b32 v138, v143, 10, v198
	ds_read_b128 v[138:141], v138
	v_lshl_or_b32 v143, v143, 8, v204
	v_mfma_f32_16x16x32_bf16 v[134:137], v[144:147], v[148:151], v[134:137]
	ds_read_b128 v[144:147], v143
	ds_read_b128 v[148:151], v216
	v_bitop3_b32 v143, v232, 7, 32 bitop3:0xde
	s_waitcnt lgkmcnt(0)
	v_mfma_f32_16x16x32_bf16 v[130:133], v[138:141], v[148:151], v[130:133]
	v_lshl_or_b32 v138, v143, 10, v198
	v_lshl_or_b32 v143, v143, 8, v204
	ds_read_b128 v[138:141], v138
	v_mfma_f32_16x16x32_bf16 v[134:137], v[144:147], v[148:151], v[134:137]
	ds_read_b128 v[144:147], v143
	ds_read_b128 v[148:151], v213
	ds_write_b64 v212, v[2:3]
	s_waitcnt vmcnt(21)
	v_cvt_pk_bf16_f32 v2, v10, v11
	v_cvt_pk_bf16_f32 v3, v12, v13
	ds_write_b64 v211, v[2:3] offset:512
	s_waitcnt vmcnt(20)
	v_cvt_pk_bf16_f32 v2, v14, v15
	v_cvt_pk_bf16_f32 v3, v16, v17
	ds_write_b64 v210, v[2:3] offset:1024
	s_waitcnt vmcnt(19)
	v_cvt_pk_bf16_f32 v2, v22, v23
	v_cvt_pk_bf16_f32 v3, v24, v25
	ds_write_b64 v209, v[2:3] offset:1536
	s_waitcnt vmcnt(18)
	v_cvt_pk_bf16_f32 v2, v30, v31
	v_cvt_pk_bf16_f32 v3, v32, v33
	ds_write_b64 v208, v[2:3] offset:2048
	s_waitcnt vmcnt(17)
	v_cvt_pk_bf16_f32 v2, v38, v39
	v_cvt_pk_bf16_f32 v3, v40, v41
	ds_write_b64 v207, v[2:3] offset:2560
	s_waitcnt vmcnt(16)
	v_cvt_pk_bf16_f32 v2, v46, v47
	v_cvt_pk_bf16_f32 v3, v48, v49
	ds_write_b64 v206, v[2:3] offset:3072
	v_cvt_pk_bf16_f32 v2, v54, v55
	v_cvt_pk_bf16_f32 v3, v56, v57
	ds_write_b64 v205, v[2:3] offset:3584
	v_cvt_pk_bf16_f32 v2, v62, v63
	v_cvt_pk_bf16_f32 v3, v64, v65
	ds_write_b64 v231, v[2:3] offset:4096
	v_cvt_pk_bf16_f32 v2, v70, v71
	v_cvt_pk_bf16_f32 v3, v72, v73
	ds_write_b64 v230, v[2:3] offset:4608
	v_cvt_pk_bf16_f32 v2, v78, v79
	v_cvt_pk_bf16_f32 v3, v80, v81
	ds_write_b64 v229, v[2:3] offset:5120
	v_cvt_pk_bf16_f32 v2, v86, v87
	v_cvt_pk_bf16_f32 v3, v88, v89
	ds_write_b64 v228, v[2:3] offset:5632
	v_cvt_pk_bf16_f32 v2, v94, v95
	v_cvt_pk_bf16_f32 v3, v96, v97
	ds_write_b64 v227, v[2:3] offset:6144
	v_cvt_pk_bf16_f32 v2, v106, v107
	v_cvt_pk_bf16_f32 v3, v108, v109
	ds_write_b64 v226, v[2:3] offset:6656
	v_cvt_pk_bf16_f32 v2, v114, v115
	v_cvt_pk_bf16_f32 v3, v116, v117
	ds_write_b64 v225, v[2:3] offset:7168
	v_cvt_pk_bf16_f32 v2, v122, v123
	v_cvt_pk_bf16_f32 v3, v124, v125
	ds_write_b64 v224, v[2:3] offset:7680
	v_lshlrev_b32_e32 v2, 10, v142
	v_and_or_b32 v2, v2, s0, v203
	v_or_b32_e32 v3, 0x2000, v2
	buffer_load_dwordx4 v[10:13], v2, s[4:7], 0 offen nt
	buffer_load_dwordx4 v[14:17], v3, s[4:7], 0 offen nt
	v_or_b32_e32 v3, 0x4000, v2
	buffer_load_dwordx4 v[22:25], v3, s[4:7], 0 offen nt
	v_or_b32_e32 v3, 0x6000, v2
	buffer_load_dwordx4 v[30:33], v3, s[4:7], 0 offen nt
	v_or_b32_e32 v3, 0x8000, v2
	buffer_load_dwordx4 v[38:41], v3, s[4:7], 0 offen nt
	v_or_b32_e32 v3, 0xa000, v2
	buffer_load_dwordx4 v[46:49], v3, s[4:7], 0 offen nt
	v_or_b32_e32 v3, 0xc000, v2
	buffer_load_dwordx4 v[54:57], v3, s[4:7], 0 offen nt
	v_or_b32_e32 v3, 0xe000, v2
	buffer_load_dwordx4 v[62:65], v3, s[4:7], 0 offen nt
	v_or_b32_e32 v3, 0x10000, v2
	buffer_load_dwordx4 v[70:73], v3, s[4:7], 0 offen nt
	v_or_b32_e32 v3, 0x12000, v2
	buffer_load_dwordx4 v[78:81], v3, s[4:7], 0 offen nt
	v_or_b32_e32 v3, 0x14000, v2
	buffer_load_dwordx4 v[86:89], v3, s[4:7], 0 offen nt
	v_or_b32_e32 v3, 0x16000, v2
	buffer_load_dwordx4 v[94:97], v3, s[4:7], 0 offen nt
	v_or_b32_e32 v3, 0x18000, v2
	buffer_load_dwordx4 v[106:109], v3, s[4:7], 0 offen nt
	v_or_b32_e32 v3, 0x1a000, v2
	buffer_load_dwordx4 v[114:117], v3, s[4:7], 0 offen nt
	v_or_b32_e32 v3, 0x1c000, v2
	v_or_b32_e32 v2, 0x1e000, v2
	s_waitcnt lgkmcnt(14)
	v_mfma_f32_16x16x32_bf16 v[138:141], v[138:141], v[148:151], v[130:133]
	buffer_load_dwordx4 v[122:125], v3, s[4:7], 0 offen nt
	s_nop 1
	buffer_load_dwordx4 v[130:133], v2, s[4:7], 0 offen nt
	v_mfma_f32_16x16x32_bf16 v[134:137], v[144:147], v[148:151], v[134:137]
	v_lshlrev_b32_e32 v2, 3, v234
	v_and_b32_e32 v143, 56, v2
	v_lshl_or_b32 v2, v143, 10, v198
	v_lshl_or_b32 v152, v143, 8, v204
	ds_read_b128 v[2:5], v2
	ds_read_b128 v[144:147], v223
	ds_read_b128 v[148:151], v222
	ds_read_b128 v[152:155], v152
	v_or_b32_e32 v156, 1, v143
	v_lshl_or_b32 v157, v156, 10, v198
	s_waitcnt lgkmcnt(2)
	v_mfma_f32_16x16x32_bf16 v[2:5], v[2:5], v[144:147], v[138:141]
	s_waitcnt vmcnt(31)
	v_cvt_pk_bf16_f32 v6, v6, v7
	v_cvt_pk_bf16_f32 v7, v8, v9
	s_waitcnt lgkmcnt(0)
	v_mfma_f32_16x16x32_bf16 v[134:137], v[152:155], v[144:147], v[134:137]
	ds_read_b128 v[138:141], v157
	v_lshl_or_b32 v144, v156, 8, v204
	ds_read_b128 v[144:147], v144
	v_or_b32_e32 v156, 2, v143
	s_waitcnt lgkmcnt(1)
	v_mfma_f32_16x16x32_bf16 v[2:5], v[138:141], v[148:151], v[2:5]
	v_lshl_or_b32 v138, v156, 10, v198
	ds_read_b128 v[138:141], v138
	ds_read_b128 v[152:155], v221
	s_waitcnt lgkmcnt(2)
	v_mfma_f32_16x16x32_bf16 v[134:137], v[144:147], v[148:151], v[134:137]
	v_lshl_or_b32 v144, v156, 8, v204
	v_or_b32_e32 v156, 3, v143
	ds_read_b128 v[144:147], v144
	ds_read_b128 v[148:151], v219
	s_waitcnt lgkmcnt(2)
	v_mfma_f32_16x16x32_bf16 v[2:5], v[138:141], v[152:155], v[2:5]
	v_lshl_or_b32 v138, v156, 10, v198
	ds_read_b128 v[138:141], v138
	s_waitcnt lgkmcnt(2)
	v_mfma_f32_16x16x32_bf16 v[134:137], v[144:147], v[152:155], v[134:137]
	v_lshl_or_b32 v144, v156, 8, v204
	ds_read_b128 v[144:147], v144
	v_or_b32_e32 v152, 4, v143
	s_waitcnt lgkmcnt(1)
	v_mfma_f32_16x16x32_bf16 v[2:5], v[138:141], v[148:151], v[2:5]
	v_lshl_or_b32 v138, v152, 10, v198
	ds_read_b128 v[138:141], v138
	v_or_b32_e32 v156, 5, v143
	s_waitcnt lgkmcnt(1)
	v_mfma_f32_16x16x32_bf16 v[134:137], v[144:147], v[148:151], v[134:137]
	ds_read_b128 v[144:147], v218
	v_lshl_or_b32 v148, v152, 8, v204
	ds_read_b128 v[148:151], v148
	ds_read_b128 v[152:155], v217
	s_waitcnt lgkmcnt(2)
	v_mfma_f32_16x16x32_bf16 v[2:5], v[138:141], v[144:147], v[2:5]
	v_lshl_or_b32 v138, v156, 10, v198
	ds_read_b128 v[138:141], v138
	s_waitcnt lgkmcnt(2)
	v_mfma_f32_16x16x32_bf16 v[134:137], v[148:151], v[144:147], v[134:137]
	v_lshl_or_b32 v144, v156, 8, v204
	ds_read_b128 v[144:147], v144
	v_or_b32_e32 v148, 6, v143
	s_waitcnt lgkmcnt(1)
	v_mfma_f32_16x16x32_bf16 v[2:5], v[138:141], v[152:155], v[2:5]
	v_lshl_or_b32 v138, v148, 10, v198
	ds_read_b128 v[138:141], v138
	v_lshl_or_b32 v148, v148, 8, v204
	s_waitcnt lgkmcnt(1)
	v_mfma_f32_16x16x32_bf16 v[134:137], v[144:147], v[152:155], v[134:137]
	ds_read_b128 v[144:147], v216
	ds_read_b128 v[148:151], v148
	ds_read_b128 v[152:155], v213
	v_or_b32_e32 v143, 7, v143
	ds_write_b64 v212, v[6:7]
	s_waitcnt lgkmcnt(3)
	v_mfma_f32_16x16x32_bf16 v[2:5], v[138:141], v[144:147], v[2:5]
	v_lshl_or_b32 v138, v143, 10, v198
	v_lshl_or_b32 v143, v143, 8, v204
	s_waitcnt vmcnt(19)
	v_cvt_pk_bf16_f32 v6, v18, v19
	v_cvt_pk_bf16_f32 v7, v20, v21
	ds_read_b128 v[138:141], v138
	s_waitcnt lgkmcnt(3)
	v_mfma_f32_16x16x32_bf16 v[134:137], v[148:151], v[144:147], v[134:137]
	ds_read_b128 v[144:147], v143
	ds_write_b64 v211, v[6:7] offset:512
	s_waitcnt vmcnt(18)
	v_cvt_pk_bf16_f32 v6, v26, v27
	v_cvt_pk_bf16_f32 v7, v28, v29
	ds_write_b64 v210, v[6:7] offset:1024
	s_waitcnt vmcnt(17)
	v_cvt_pk_bf16_f32 v6, v34, v35
	v_cvt_pk_bf16_f32 v7, v36, v37
	ds_write_b64 v209, v[6:7] offset:1536
	s_waitcnt vmcnt(16)
	v_cvt_pk_bf16_f32 v6, v42, v43
	v_cvt_pk_bf16_f32 v7, v44, v45
	ds_write_b64 v208, v[6:7] offset:2048
	v_cvt_pk_bf16_f32 v6, v50, v51
	v_cvt_pk_bf16_f32 v7, v52, v53
	ds_write_b64 v207, v[6:7] offset:2560
	v_cvt_pk_bf16_f32 v6, v58, v59
	v_cvt_pk_bf16_f32 v7, v60, v61
	ds_write_b64 v206, v[6:7] offset:3072
	v_cvt_pk_bf16_f32 v6, v66, v67
	v_cvt_pk_bf16_f32 v7, v68, v69
	ds_write_b64 v205, v[6:7] offset:3584
	v_cvt_pk_bf16_f32 v6, v74, v75
	v_cvt_pk_bf16_f32 v7, v76, v77
	ds_write_b64 v231, v[6:7] offset:4096
	v_cvt_pk_bf16_f32 v6, v82, v83
	v_cvt_pk_bf16_f32 v7, v84, v85
	ds_write_b64 v230, v[6:7] offset:4608
	v_cvt_pk_bf16_f32 v6, v90, v91
	v_cvt_pk_bf16_f32 v7, v92, v93
	s_waitcnt lgkmcnt(9)
	v_mfma_f32_16x16x32_bf16 v[134:137], v[144:147], v[152:155], v[134:137]
	ds_write_b64 v229, v[6:7] offset:5120
	v_cvt_pk_bf16_f32 v6, v98, v99
	v_cvt_pk_bf16_f32 v7, v100, v101
	ds_write_b64 v228, v[6:7] offset:5632
	v_cvt_pk_bf16_f32 v6, v102, v103
	v_cvt_pk_bf16_f32 v7, v104, v105
	ds_write_b64 v227, v[6:7] offset:6144
	v_cvt_pk_bf16_f32 v6, v110, v111
	v_cvt_pk_bf16_f32 v7, v112, v113
	ds_write_b64 v226, v[6:7] offset:6656
	v_cvt_pk_bf16_f32 v6, v118, v119
	v_cvt_pk_bf16_f32 v7, v120, v121
	v_mfma_f32_16x16x32_bf16 v[2:5], v[138:141], v[152:155], v[2:5]
	ds_write_b64 v225, v[6:7] offset:7168
	v_cvt_pk_bf16_f32 v6, v126, v127
	v_cvt_pk_bf16_f32 v7, v128, v129
	ds_write_b64 v224, v[6:7] offset:7680
	v_add_u32_e32 v6, 48, v232
	v_and_b32_e32 v50, 56, v6
	v_lshl_or_b32 v6, v50, 10, v198
	v_lshl_or_b32 v34, v50, 8, v204
	ds_read_b128 v[6:9], v6
	ds_read_b128 v[18:21], v223
	ds_read_b128 v[26:29], v222
	ds_read_b128 v[34:37], v34
	v_or_b32_e32 v42, 1, v50
	v_lshl_or_b32 v43, v42, 10, v198
	s_waitcnt lgkmcnt(2)
	v_mfma_f32_16x16x32_bf16 v[2:5], v[6:9], v[18:21], v[2:5]
	ds_read_b128 v[6:9], v43
	v_or_b32_e32 v51, 2, v50
	s_waitcnt lgkmcnt(1)
	v_mfma_f32_16x16x32_bf16 v[18:21], v[34:37], v[18:21], v[134:137]
	v_lshl_or_b32 v34, v42, 8, v204
	ds_read_b128 v[34:37], v34
	s_waitcnt lgkmcnt(1)
	v_mfma_f32_16x16x32_bf16 v[2:5], v[6:9], v[26:29], v[2:5]
	v_lshl_or_b32 v6, v51, 10, v198
	ds_read_b128 v[6:9], v6
	ds_read_b128 v[42:45], v221
	s_waitcnt lgkmcnt(2)
	v_mfma_f32_16x16x32_bf16 v[18:21], v[34:37], v[26:29], v[18:21]
	v_lshl_or_b32 v26, v51, 8, v204
	v_or_b32_e32 v51, 3, v50
	ds_read_b128 v[26:29], v26
	ds_read_b128 v[34:37], v219
	s_waitcnt lgkmcnt(2)
	v_mfma_f32_16x16x32_bf16 v[2:5], v[6:9], v[42:45], v[2:5]
	v_lshl_or_b32 v6, v51, 10, v198
	ds_read_b128 v[6:9], v6
	s_waitcnt lgkmcnt(2)
	v_mfma_f32_16x16x32_bf16 v[18:21], v[26:29], v[42:45], v[18:21]
	v_lshl_or_b32 v26, v51, 8, v204
	ds_read_b128 v[26:29], v26
	v_or_b32_e32 v42, 4, v50
	s_waitcnt lgkmcnt(1)
	v_mfma_f32_16x16x32_bf16 v[2:5], v[6:9], v[34:37], v[2:5]
	v_lshl_or_b32 v6, v42, 10, v198
	ds_read_b128 v[6:9], v6
	v_or_b32_e32 v51, 5, v50
	s_waitcnt lgkmcnt(1)
	v_mfma_f32_16x16x32_bf16 v[18:21], v[26:29], v[34:37], v[18:21]
	ds_read_b128 v[26:29], v218
	v_lshl_or_b32 v34, v42, 8, v204
	ds_read_b128 v[34:37], v34
	ds_read_b128 v[42:45], v217
	s_waitcnt lgkmcnt(2)
	v_mfma_f32_16x16x32_bf16 v[2:5], v[6:9], v[26:29], v[2:5]
	v_lshl_or_b32 v6, v51, 10, v198
	ds_read_b128 v[6:9], v6
	s_waitcnt lgkmcnt(2)
	v_mfma_f32_16x16x32_bf16 v[18:21], v[34:37], v[26:29], v[18:21]
	v_lshl_or_b32 v26, v51, 8, v204
	ds_read_b128 v[26:29], v26
	v_or_b32_e32 v34, 6, v50
	s_waitcnt lgkmcnt(1)
	v_mfma_f32_16x16x32_bf16 v[2:5], v[6:9], v[42:45], v[2:5]
	v_lshl_or_b32 v6, v34, 10, v198
	ds_read_b128 v[6:9], v6
	v_lshl_or_b32 v34, v34, 8, v204
	s_waitcnt lgkmcnt(1)
	v_mfma_f32_16x16x32_bf16 v[18:21], v[26:29], v[42:45], v[18:21]
	ds_read_b128 v[26:29], v216
	ds_read_b128 v[34:37], v34
	ds_read_b128 v[42:45], v213
	v_or_b32_e32 v50, 7, v50
	s_waitcnt lgkmcnt(2)
	v_mfma_f32_16x16x32_bf16 v[2:5], v[6:9], v[26:29], v[2:5]
	v_lshl_or_b32 v6, v50, 10, v198
	ds_read_b128 v[6:9], v6
	s_waitcnt lgkmcnt(2)
	v_mfma_f32_16x16x32_bf16 v[18:21], v[34:37], v[26:29], v[18:21]
	v_lshl_or_b32 v26, v50, 8, v204
	ds_read_b128 v[26:29], v26
	s_waitcnt lgkmcnt(1)
	v_mfma_f32_16x16x32_bf16 v[34:37], v[6:9], v[42:45], v[2:5]
	v_and_b32_e32 v74, 7, v197
	v_lshrrev_b32_e32 v75, 3, v197
	v_lshlrev_b32_e32 v192, 13, v200
	v_lshlrev_b32_e32 v193, 11, v200
	v_lshl_add_u32 v203, v197, 2, v196
	v_lshl_or_b32 v192, v75, 8, v192
	v_lshl_or_b32 v193, v75, 6, v193
	v_add_u32_e32 v203, 0x24800, v203
	v_lshl_or_b32 v192, v201, 6, v192
	v_lshl_or_b32 v193, v74, 1, v193
	v_lshl_or_b32 v192, v74, 1, v192
	v_or_b32_e32 v193, 0x10000, v193
	v_cmp_gt_u32_e64 s[36:37], 16, v1
	v_cmp_eq_u32_e64 s[38:39], 1, v201
	ds_read2_b32 v[2:3], v203 offset1:16
	ds_read2_b32 v[4:5], v203 offset0:32 offset1:48
	ds_read2_b32 v[6:7], v203 offset0:64 offset1:80
	ds_read2_b32 v[8:9], v203 offset0:96 offset1:112
	ds_read2_b32 v[50:51], v203 offset0:128 offset1:144
	ds_read2_b32 v[52:53], v203 offset0:160 offset1:176
	ds_read2_b32 v[58:59], v203 offset0:192 offset1:208
	ds_read2_b32 v[60:61], v203 offset0:224 offset1:240
	v_mov_b32_e32 v146, 0
	v_mov_b32_e32 v147, 0
	v_mov_b32_e32 v150, 0
	v_mov_b32_e32 v151, 0
	v_mov_b32_e32 v154, 0
	v_mov_b32_e32 v155, 0
	v_mov_b32_e32 v158, 0
	v_mov_b32_e32 v159, 0
	v_mov_b32_e32 v162, 0
	v_mov_b32_e32 v163, 0
	v_mov_b32_e32 v166, 0
	v_mov_b32_e32 v167, 0
	v_mov_b32_e32 v170, 0
	v_mov_b32_e32 v171, 0
	v_mov_b32_e32 v174, 0
	v_mov_b32_e32 v175, 0
	v_mov_b32_e32 v178, 0
	v_mov_b32_e32 v179, 0
	v_mov_b32_e32 v182, 0
	v_mov_b32_e32 v183, 0
	v_mov_b32_e32 v186, 0
	v_mov_b32_e32 v187, 0
	v_mov_b32_e32 v190, 0
	v_mov_b32_e32 v191, 0
	v_mov_b32_e32 v234, 0
	v_mov_b32_e32 v235, 0
	v_mov_b32_e32 v238, 0
	v_mov_b32_e32 v239, 0
	v_mov_b32_e32 v242, 0
	v_mov_b32_e32 v243, 0
	v_mov_b32_e32 v246, 0
	v_mov_b32_e32 v247, 0
	ds_read_u16 v82, v192
	ds_read_u16 v83, v192 offset:16
	ds_read_u16 v84, v192 offset:32
	ds_read_u16 v85, v192 offset:48
	ds_read_u16 v90, v193
	ds_read_u16 v91, v193 offset:16
	ds_read_u16 v92, v193 offset:32
	ds_read_u16 v93, v193 offset:48
	ds_read_u16 v98, v192 offset:512
	ds_read_u16 v99, v192 offset:528
	ds_read_u16 v100, v192 offset:544
	ds_read_u16 v101, v192 offset:560
	ds_read_u16 v102, v193 offset:128
	ds_read_u16 v103, v193 offset:144
	ds_read_u16 v104, v193 offset:160
	ds_read_u16 v105, v193 offset:176
	s_waitcnt lgkmcnt(8)
	v_lshl_or_b32 v144, v83, 16, v82
	v_lshl_or_b32 v145, v85, 16, v84
	s_mov_b64 exec, s[36:37]
	v_lshl_or_b32 v146, v91, 16, v90
	v_lshl_or_b32 v147, v93, 16, v92
	s_mov_b64 exec, -1
	ds_read_u16 v82, v192 offset:1024
	ds_read_u16 v83, v192 offset:1040
	ds_read_u16 v84, v192 offset:1056
	ds_read_u16 v85, v192 offset:1072
	ds_read_u16 v90, v193 offset:256
	ds_read_u16 v91, v193 offset:272
	ds_read_u16 v92, v193 offset:288
	ds_read_u16 v93, v193 offset:304
	s_waitcnt lgkmcnt(8)
	v_lshl_or_b32 v148, v99, 16, v98
	v_lshl_or_b32 v149, v101, 16, v100
	s_mov_b64 exec, s[36:37]
	v_lshl_or_b32 v150, v103, 16, v102
	v_lshl_or_b32 v151, v105, 16, v104
	s_mov_b64 exec, -1
	ds_read_u16 v98, v192 offset:1536
	ds_read_u16 v99, v192 offset:1552
	ds_read_u16 v100, v192 offset:1568
	ds_read_u16 v101, v192 offset:1584
	ds_read_u16 v102, v193 offset:384
	ds_read_u16 v103, v193 offset:400
	ds_read_u16 v104, v193 offset:416
	ds_read_u16 v105, v193 offset:432
	s_waitcnt lgkmcnt(8)
	v_lshl_or_b32 v152, v83, 16, v82
	v_lshl_or_b32 v153, v85, 16, v84
	s_mov_b64 exec, s[36:37]
	v_lshl_or_b32 v154, v91, 16, v90
	v_lshl_or_b32 v155, v93, 16, v92
	s_mov_b64 exec, -1
	ds_read_u16 v82, v192 offset:2048
	ds_read_u16 v83, v192 offset:2064
	ds_read_u16 v84, v192 offset:2080
	ds_read_u16 v85, v192 offset:2096
	ds_read_u16 v90, v193 offset:512
	ds_read_u16 v91, v193 offset:528
	ds_read_u16 v92, v193 offset:544
	ds_read_u16 v93, v193 offset:560
	s_waitcnt lgkmcnt(8)
	v_lshl_or_b32 v156, v99, 16, v98
	v_lshl_or_b32 v157, v101, 16, v100
	s_mov_b64 exec, s[36:37]
	v_lshl_or_b32 v158, v103, 16, v102
	v_lshl_or_b32 v159, v105, 16, v104
	s_mov_b64 exec, -1
	ds_read_u16 v98, v192 offset:2560
	ds_read_u16 v99, v192 offset:2576
	ds_read_u16 v100, v192 offset:2592
	ds_read_u16 v101, v192 offset:2608
	ds_read_u16 v102, v193 offset:640
	ds_read_u16 v103, v193 offset:656
	ds_read_u16 v104, v193 offset:672
	ds_read_u16 v105, v193 offset:688
	s_waitcnt lgkmcnt(8)
	v_lshl_or_b32 v160, v83, 16, v82
	v_lshl_or_b32 v161, v85, 16, v84
	s_mov_b64 exec, s[36:37]
	v_lshl_or_b32 v162, v91, 16, v90
	v_lshl_or_b32 v163, v93, 16, v92
	s_mov_b64 exec, -1
	ds_read_u16 v82, v192 offset:3072
	ds_read_u16 v83, v192 offset:3088
	ds_read_u16 v84, v192 offset:3104
	ds_read_u16 v85, v192 offset:3120
	ds_read_u16 v90, v193 offset:768
	ds_read_u16 v91, v193 offset:784
	ds_read_u16 v92, v193 offset:800
	ds_read_u16 v93, v193 offset:816
	s_waitcnt lgkmcnt(8)
	v_lshl_or_b32 v164, v99, 16, v98
	v_lshl_or_b32 v165, v101, 16, v100
	s_mov_b64 exec, s[36:37]
	v_lshl_or_b32 v166, v103, 16, v102
	v_lshl_or_b32 v167, v105, 16, v104
	s_mov_b64 exec, -1
	ds_read_u16 v98, v192 offset:3584
	ds_read_u16 v99, v192 offset:3600
	ds_read_u16 v100, v192 offset:3616
	ds_read_u16 v101, v192 offset:3632
	ds_read_u16 v102, v193 offset:896
	ds_read_u16 v103, v193 offset:912
	ds_read_u16 v104, v193 offset:928
	ds_read_u16 v105, v193 offset:944
	s_waitcnt lgkmcnt(8)
	v_lshl_or_b32 v168, v83, 16, v82
	v_lshl_or_b32 v169, v85, 16, v84
	s_mov_b64 exec, s[36:37]
	v_lshl_or_b32 v170, v91, 16, v90
	v_lshl_or_b32 v171, v93, 16, v92
	s_mov_b64 exec, -1
	ds_read_u16 v82, v192 offset:4096
	ds_read_u16 v83, v192 offset:4112
	ds_read_u16 v84, v192 offset:4128
	ds_read_u16 v85, v192 offset:4144
	ds_read_u16 v90, v193 offset:1024
	ds_read_u16 v91, v193 offset:1040
	ds_read_u16 v92, v193 offset:1056
	ds_read_u16 v93, v193 offset:1072
	s_waitcnt lgkmcnt(8)
	v_lshl_or_b32 v172, v99, 16, v98
	v_lshl_or_b32 v173, v101, 16, v100
	s_mov_b64 exec, s[36:37]
	v_lshl_or_b32 v174, v103, 16, v102
	v_lshl_or_b32 v175, v105, 16, v104
	s_mov_b64 exec, -1
	ds_read_u16 v98, v192 offset:4608
	ds_read_u16 v99, v192 offset:4624
	ds_read_u16 v100, v192 offset:4640
	ds_read_u16 v101, v192 offset:4656
	ds_read_u16 v102, v193 offset:1152
	ds_read_u16 v103, v193 offset:1168
	ds_read_u16 v104, v193 offset:1184
	ds_read_u16 v105, v193 offset:1200
	s_waitcnt lgkmcnt(8)
	v_lshl_or_b32 v176, v83, 16, v82
	v_lshl_or_b32 v177, v85, 16, v84
	s_mov_b64 exec, s[36:37]
	v_lshl_or_b32 v178, v91, 16, v90
	v_lshl_or_b32 v179, v93, 16, v92
	s_mov_b64 exec, -1
	ds_read_u16 v82, v192 offset:5120
	ds_read_u16 v83, v192 offset:5136
	ds_read_u16 v84, v192 offset:5152
	ds_read_u16 v85, v192 offset:5168
	ds_read_u16 v90, v193 offset:1280
	ds_read_u16 v91, v193 offset:1296
	ds_read_u16 v92, v193 offset:1312
	ds_read_u16 v93, v193 offset:1328
	s_waitcnt lgkmcnt(8)
	v_lshl_or_b32 v180, v99, 16, v98
	v_lshl_or_b32 v181, v101, 16, v100
	s_mov_b64 exec, s[36:37]
	v_lshl_or_b32 v182, v103, 16, v102
	v_lshl_or_b32 v183, v105, 16, v104
	s_mov_b64 exec, -1
	ds_read_u16 v98, v192 offset:5632
	ds_read_u16 v99, v192 offset:5648
	ds_read_u16 v100, v192 offset:5664
	ds_read_u16 v101, v192 offset:5680
	ds_read_u16 v102, v193 offset:1408
	ds_read_u16 v103, v193 offset:1424
	ds_read_u16 v104, v193 offset:1440
	ds_read_u16 v105, v193 offset:1456
	s_waitcnt lgkmcnt(8)
	v_lshl_or_b32 v184, v83, 16, v82
	v_lshl_or_b32 v185, v85, 16, v84
	s_mov_b64 exec, s[36:37]
	v_lshl_or_b32 v186, v91, 16, v90
	v_lshl_or_b32 v187, v93, 16, v92
	s_mov_b64 exec, -1
	ds_read_u16 v82, v192 offset:6144
	ds_read_u16 v83, v192 offset:6160
	ds_read_u16 v84, v192 offset:6176
	ds_read_u16 v85, v192 offset:6192
	ds_read_u16 v90, v193 offset:1536
	ds_read_u16 v91, v193 offset:1552
	ds_read_u16 v92, v193 offset:1568
	ds_read_u16 v93, v193 offset:1584
	s_waitcnt lgkmcnt(8)
	v_lshl_or_b32 v188, v99, 16, v98
	v_lshl_or_b32 v189, v101, 16, v100
	s_mov_b64 exec, s[36:37]
	v_lshl_or_b32 v190, v103, 16, v102
	v_lshl_or_b32 v191, v105, 16, v104
	s_mov_b64 exec, -1
	ds_read_u16 v98, v192 offset:6656
	ds_read_u16 v99, v192 offset:6672
	ds_read_u16 v100, v192 offset:6688
	ds_read_u16 v101, v192 offset:6704
	ds_read_u16 v102, v193 offset:1664
	ds_read_u16 v103, v193 offset:1680
	ds_read_u16 v104, v193 offset:1696
	ds_read_u16 v105, v193 offset:1712
	s_waitcnt lgkmcnt(8)
	v_lshl_or_b32 v232, v83, 16, v82
	v_lshl_or_b32 v233, v85, 16, v84
	s_mov_b64 exec, s[36:37]
	v_lshl_or_b32 v234, v91, 16, v90
	v_lshl_or_b32 v235, v93, 16, v92
	s_mov_b64 exec, -1
	ds_read_u16 v82, v192 offset:7168
	ds_read_u16 v83, v192 offset:7184
	ds_read_u16 v84, v192 offset:7200
	ds_read_u16 v85, v192 offset:7216
	ds_read_u16 v90, v193 offset:1792
	ds_read_u16 v91, v193 offset:1808
	ds_read_u16 v92, v193 offset:1824
	ds_read_u16 v93, v193 offset:1840
	s_waitcnt lgkmcnt(8)
	v_lshl_or_b32 v236, v99, 16, v98
	v_lshl_or_b32 v237, v101, 16, v100
	s_mov_b64 exec, s[36:37]
	v_lshl_or_b32 v238, v103, 16, v102
	v_lshl_or_b32 v239, v105, 16, v104
	s_mov_b64 exec, -1
	ds_read_u16 v98, v192 offset:7680
	ds_read_u16 v99, v192 offset:7696
	ds_read_u16 v100, v192 offset:7712
	ds_read_u16 v101, v192 offset:7728
	ds_read_u16 v102, v193 offset:1920
	ds_read_u16 v103, v193 offset:1936
	ds_read_u16 v104, v193 offset:1952
	ds_read_u16 v105, v193 offset:1968
	s_waitcnt lgkmcnt(8)
	v_lshl_or_b32 v240, v83, 16, v82
	v_lshl_or_b32 v241, v85, 16, v84
	s_mov_b64 exec, s[36:37]
	v_lshl_or_b32 v242, v91, 16, v90
	v_lshl_or_b32 v243, v93, 16, v92
	s_mov_b64 exec, -1
	s_waitcnt lgkmcnt(0)
	v_lshl_or_b32 v244, v99, 16, v98
	v_lshl_or_b32 v245, v101, 16, v100
	s_mov_b64 exec, s[36:37]
	v_lshl_or_b32 v246, v103, 16, v102
	v_lshl_or_b32 v247, v105, 16, v104
	s_mov_b64 exec, -1
	s_waitcnt lgkmcnt(0)
	s_mov_b64 exec, s[38:39]
	v_cvt_pk_bf16_f32 v66, v2, v195
	v_cvt_pk_bf16_f32 v74, v3, v195
	v_lshlrev_b32_e32 v67, 16, v66
	v_lshlrev_b32_e32 v75, 16, v74
	v_sub_f32_e32 v2, v2, v67
	v_sub_f32_e32 v3, v3, v75
	v_cvt_pk_bf16_f32 v68, v2, v195
	v_cvt_pk_bf16_f32 v76, v3, v195
	v_lshlrev_b32_e32 v69, 16, v68
	v_lshlrev_b32_e32 v77, 16, v76
	v_sub_f32_e32 v2, v2, v69
	v_sub_f32_e32 v3, v3, v77
	v_cvt_pk_bf16_f32 v147, v2, v195
	v_cvt_pk_bf16_f32 v151, v3, v195
	v_cvt_pk_bf16_f32 v146, v67, v69
	v_cvt_pk_bf16_f32 v150, v75, v77
	v_cvt_pk_bf16_f32 v66, v4, v195
	v_cvt_pk_bf16_f32 v74, v5, v195
	v_lshlrev_b32_e32 v67, 16, v66
	v_lshlrev_b32_e32 v75, 16, v74
	v_sub_f32_e32 v4, v4, v67
	v_sub_f32_e32 v5, v5, v75
	v_cvt_pk_bf16_f32 v68, v4, v195
	v_cvt_pk_bf16_f32 v76, v5, v195
	v_lshlrev_b32_e32 v69, 16, v68
	v_lshlrev_b32_e32 v77, 16, v76
	v_sub_f32_e32 v4, v4, v69
	v_sub_f32_e32 v5, v5, v77
	v_cvt_pk_bf16_f32 v155, v4, v195
	v_cvt_pk_bf16_f32 v159, v5, v195
	v_cvt_pk_bf16_f32 v154, v67, v69
	v_cvt_pk_bf16_f32 v158, v75, v77
	v_cvt_pk_bf16_f32 v66, v6, v195
	v_cvt_pk_bf16_f32 v74, v7, v195
	v_lshlrev_b32_e32 v67, 16, v66
	v_lshlrev_b32_e32 v75, 16, v74
	v_sub_f32_e32 v6, v6, v67
	v_sub_f32_e32 v7, v7, v75
	v_cvt_pk_bf16_f32 v68, v6, v195
	v_cvt_pk_bf16_f32 v76, v7, v195
	v_lshlrev_b32_e32 v69, 16, v68
	v_lshlrev_b32_e32 v77, 16, v76
	v_sub_f32_e32 v6, v6, v69
	v_sub_f32_e32 v7, v7, v77
	v_cvt_pk_bf16_f32 v163, v6, v195
	v_cvt_pk_bf16_f32 v167, v7, v195
	v_cvt_pk_bf16_f32 v162, v67, v69
	v_cvt_pk_bf16_f32 v166, v75, v77
	v_cvt_pk_bf16_f32 v66, v8, v195
	v_cvt_pk_bf16_f32 v74, v9, v195
	v_lshlrev_b32_e32 v67, 16, v66
	v_lshlrev_b32_e32 v75, 16, v74
	v_sub_f32_e32 v8, v8, v67
	v_sub_f32_e32 v9, v9, v75
	v_cvt_pk_bf16_f32 v68, v8, v195
	v_cvt_pk_bf16_f32 v76, v9, v195
	v_lshlrev_b32_e32 v69, 16, v68
	v_lshlrev_b32_e32 v77, 16, v76
	v_sub_f32_e32 v8, v8, v69
	v_sub_f32_e32 v9, v9, v77
	v_cvt_pk_bf16_f32 v171, v8, v195
	v_cvt_pk_bf16_f32 v175, v9, v195
	v_cvt_pk_bf16_f32 v170, v67, v69
	v_cvt_pk_bf16_f32 v174, v75, v77
	v_cvt_pk_bf16_f32 v66, v50, v195
	v_cvt_pk_bf16_f32 v74, v51, v195
	v_lshlrev_b32_e32 v67, 16, v66
	v_lshlrev_b32_e32 v75, 16, v74
	v_sub_f32_e32 v50, v50, v67
	v_sub_f32_e32 v51, v51, v75
	v_cvt_pk_bf16_f32 v68, v50, v195
	v_cvt_pk_bf16_f32 v76, v51, v195
	v_lshlrev_b32_e32 v69, 16, v68
	v_lshlrev_b32_e32 v77, 16, v76
	v_sub_f32_e32 v50, v50, v69
	v_sub_f32_e32 v51, v51, v77
	v_cvt_pk_bf16_f32 v179, v50, v195
	v_cvt_pk_bf16_f32 v183, v51, v195
	v_cvt_pk_bf16_f32 v178, v67, v69
	v_cvt_pk_bf16_f32 v182, v75, v77
	v_cvt_pk_bf16_f32 v66, v52, v195
	v_cvt_pk_bf16_f32 v74, v53, v195
	v_lshlrev_b32_e32 v67, 16, v66
	v_lshlrev_b32_e32 v75, 16, v74
	v_sub_f32_e32 v52, v52, v67
	v_sub_f32_e32 v53, v53, v75
	v_cvt_pk_bf16_f32 v68, v52, v195
	v_cvt_pk_bf16_f32 v76, v53, v195
	v_lshlrev_b32_e32 v69, 16, v68
	v_lshlrev_b32_e32 v77, 16, v76
	v_sub_f32_e32 v52, v52, v69
	v_sub_f32_e32 v53, v53, v77
	v_cvt_pk_bf16_f32 v187, v52, v195
	v_cvt_pk_bf16_f32 v191, v53, v195
	v_cvt_pk_bf16_f32 v186, v67, v69
	v_cvt_pk_bf16_f32 v190, v75, v77
	v_cvt_pk_bf16_f32 v66, v58, v195
	v_cvt_pk_bf16_f32 v74, v59, v195
	v_lshlrev_b32_e32 v67, 16, v66
	v_lshlrev_b32_e32 v75, 16, v74
	v_sub_f32_e32 v58, v58, v67
	v_sub_f32_e32 v59, v59, v75
	v_cvt_pk_bf16_f32 v68, v58, v195
	v_cvt_pk_bf16_f32 v76, v59, v195
	v_lshlrev_b32_e32 v69, 16, v68
	v_lshlrev_b32_e32 v77, 16, v76
	v_sub_f32_e32 v58, v58, v69
	v_sub_f32_e32 v59, v59, v77
	v_cvt_pk_bf16_f32 v235, v58, v195
	v_cvt_pk_bf16_f32 v239, v59, v195
	v_cvt_pk_bf16_f32 v234, v67, v69
	v_cvt_pk_bf16_f32 v238, v75, v77
	v_cvt_pk_bf16_f32 v66, v60, v195
	v_cvt_pk_bf16_f32 v74, v61, v195
	v_lshlrev_b32_e32 v67, 16, v66
	v_lshlrev_b32_e32 v75, 16, v74
	v_sub_f32_e32 v60, v60, v67
	v_sub_f32_e32 v61, v61, v75
	v_cvt_pk_bf16_f32 v68, v60, v195
	v_cvt_pk_bf16_f32 v76, v61, v195
	v_lshlrev_b32_e32 v69, 16, v68
	v_lshlrev_b32_e32 v77, 16, v76
	v_sub_f32_e32 v60, v60, v69
	v_sub_f32_e32 v61, v61, v77
	v_cvt_pk_bf16_f32 v243, v60, v195
	v_cvt_pk_bf16_f32 v247, v61, v195
	v_cvt_pk_bf16_f32 v242, v67, v69
	v_cvt_pk_bf16_f32 v246, v75, v77
	s_mov_b64 exec, -1
	s_waitcnt vmcnt(15)
	v_cvt_pk_bf16_f32 v6, v10, v11
	v_cvt_pk_bf16_f32 v7, v12, v13
	ds_write_b64 v212, v[6:7]
	s_waitcnt vmcnt(14)
	v_cvt_pk_bf16_f32 v6, v14, v15
	v_cvt_pk_bf16_f32 v7, v16, v17
	ds_write_b64 v211, v[6:7] offset:512
	s_waitcnt vmcnt(13)
	v_cvt_pk_bf16_f32 v6, v22, v23
	v_cvt_pk_bf16_f32 v7, v24, v25
	ds_write_b64 v210, v[6:7] offset:1024
	s_waitcnt vmcnt(12)
	v_cvt_pk_bf16_f32 v6, v30, v31
	v_cvt_pk_bf16_f32 v7, v32, v33
	ds_write_b64 v209, v[6:7] offset:1536
	s_waitcnt vmcnt(11)
	v_cvt_pk_bf16_f32 v6, v38, v39
	v_cvt_pk_bf16_f32 v7, v40, v41
	ds_write_b64 v208, v[6:7] offset:2048
	s_waitcnt vmcnt(10)
	v_cvt_pk_bf16_f32 v6, v46, v47
	v_cvt_pk_bf16_f32 v7, v48, v49
	ds_write_b64 v207, v[6:7] offset:2560
	s_waitcnt vmcnt(9)
	v_cvt_pk_bf16_f32 v6, v54, v55
	v_cvt_pk_bf16_f32 v7, v56, v57
	ds_write_b64 v206, v[6:7] offset:3072
	s_waitcnt vmcnt(8)
	v_cvt_pk_bf16_f32 v6, v62, v63
	v_cvt_pk_bf16_f32 v7, v64, v65
	ds_write_b64 v205, v[6:7] offset:3584
	s_waitcnt vmcnt(7)
	v_cvt_pk_bf16_f32 v6, v70, v71
	v_cvt_pk_bf16_f32 v7, v72, v73
	ds_write_b64 v231, v[6:7] offset:4096
	s_waitcnt vmcnt(6)
	v_cvt_pk_bf16_f32 v6, v78, v79
	v_cvt_pk_bf16_f32 v7, v80, v81
	ds_write_b64 v230, v[6:7] offset:4608
	s_waitcnt vmcnt(5)
	v_cvt_pk_bf16_f32 v6, v86, v87
	v_cvt_pk_bf16_f32 v7, v88, v89
	ds_write_b64 v229, v[6:7] offset:5120
	s_waitcnt vmcnt(4)
	v_cvt_pk_bf16_f32 v6, v94, v95
	v_cvt_pk_bf16_f32 v7, v96, v97
	ds_write_b64 v228, v[6:7] offset:5632
	s_waitcnt vmcnt(3)
	v_cvt_pk_bf16_f32 v6, v106, v107
	v_cvt_pk_bf16_f32 v7, v108, v109
	ds_write_b64 v227, v[6:7] offset:6144
	s_waitcnt vmcnt(2)
	v_cvt_pk_bf16_f32 v6, v114, v115
	v_cvt_pk_bf16_f32 v7, v116, v117
	ds_write_b64 v226, v[6:7] offset:6656
	s_waitcnt vmcnt(1)
	v_cvt_pk_bf16_f32 v6, v122, v123
	v_cvt_pk_bf16_f32 v7, v124, v125
	s_waitcnt lgkmcnt(14)
	v_mfma_f32_16x16x32_bf16 v[2:5], v[26:29], v[42:45], v[18:21]
	ds_write_b64 v225, v[6:7] offset:7168
	s_waitcnt vmcnt(0)
	v_cvt_pk_bf16_f32 v6, v130, v131
	v_cvt_pk_bf16_f32 v7, v132, v133
	ds_write_b64 v224, v[6:7] offset:7680
	v_lshlrev_b32_e32 v6, 3, v142
	v_and_b32_e32 v58, 56, v6
	v_lshl_or_b32 v6, v58, 10, v198
	v_or_b32_e32 v18, 1, v58
	v_lshl_or_b32 v7, v58, 8, v204
	ds_read_b128 v[14:17], v6
	ds_read_b128 v[10:13], v7
	v_lshl_or_b32 v6, v18, 10, v198
	ds_read_b128 v[26:29], v6
	ds_read_b128 v[22:25], v223
	ds_read_b128 v[6:9], v222
	v_or_b32_e32 v42, 2, v58
	v_lshl_or_b32 v19, v42, 10, v198
	ds_read_b128 v[38:41], v19
	s_waitcnt lgkmcnt(2)
	v_mfma_f32_16x16x32_bf16 v[30:33], v[14:17], v[22:25], v[34:37]
	v_lshl_or_b32 v14, v18, 8, v204
	ds_read_b128 v[18:21], v14
	ds_read_b128 v[14:17], v221
	v_or_b32_e32 v59, 5, v58
	s_waitcnt lgkmcnt(3)
	v_mfma_f32_16x16x32_bf16 v[34:37], v[26:29], v[6:9], v[30:33]
	v_lshl_or_b32 v26, v42, 8, v204
	ds_read_b128 v[26:29], v26
	s_nop 0
	ds_read_b128 v[30:33], v219
	v_or_b32_e32 v68, 6, v58
	s_waitcnt lgkmcnt(2)
	v_mfma_f32_16x16x32_bf16 v[38:41], v[38:41], v[14:17], v[34:37]
	v_lshl_or_b32 v64, v68, 10, v198
	s_nop 1
	v_or_b32_e32 v34, 3, v58
	v_lshl_or_b32 v35, v34, 10, v198
	ds_read_b128 v[42:45], v35
	v_lshl_or_b32 v34, v34, 8, v204
	s_waitcnt lgkmcnt(0)
	v_mfma_f32_16x16x32_bf16 v[46:49], v[42:45], v[30:33], v[38:41]
	s_nop 2
	v_or_b32_e32 v38, 4, v58
	v_lshl_or_b32 v39, v38, 10, v198
	v_lshl_or_b32 v38, v38, 8, v204
	ds_read_b128 v[34:37], v34
	ds_read_b128 v[50:53], v39
	ds_read_b128 v[42:45], v38
	v_lshl_or_b32 v38, v59, 10, v198
	ds_read_b128 v[54:57], v38
	ds_read_b128 v[60:63], v218
	ds_read_b128 v[38:41], v217
	ds_read_b128 v[72:75], v64
	s_waitcnt lgkmcnt(2)
	v_mfma_f32_16x16x32_bf16 v[64:67], v[50:53], v[60:63], v[46:49]
	v_or_b32_e32 v58, 7, v58
	s_nop 1
	v_lshl_or_b32 v46, v59, 8, v204
	v_lshl_or_b32 v59, v68, 8, v204
	ds_read_b128 v[50:53], v46
	ds_read_b128 v[46:49], v216
	s_waitcnt lgkmcnt(3)
	v_mfma_f32_16x16x32_bf16 v[54:57], v[54:57], v[38:41], v[64:67]
	s_nop 2
	ds_read_b128 v[64:67], v59
	ds_read_b128 v[68:71], v213
	v_lshl_or_b32 v59, v58, 10, v198
	ds_read_b128 v[76:79], v59
	s_waitcnt lgkmcnt(3)
	v_mfma_f32_16x16x32_bf16 v[54:57], v[72:75], v[46:49], v[54:57]
	v_lshl_or_b32 v58, v58, 8, v204
	ds_read_b128 v[72:75], v58
	s_waitcnt lgkmcnt(1)
	v_mfma_f32_16x16x32_bf16 v[56:59], v[76:79], v[68:71], v[54:57]
	s_nop 2
	v_add_u32_e32 v76, 0x24800, v196
	s_waitcnt lgkmcnt(0)
	v_mfma_f32_16x16x32_bf16 v[2:5], v[10:13], v[22:25], v[2:5]
	v_mfma_f32_16x16x32_bf16 v[2:5], v[18:21], v[6:9], v[2:5]
	s_waitcnt lgkmcnt(0)
	v_mfma_f32_16x16x32_bf16 v[2:5], v[26:29], v[14:17], v[2:5]
	v_mfma_f32_16x16x32_bf16 v[2:5], v[34:37], v[30:33], v[2:5]
	s_waitcnt lgkmcnt(0)
	v_mfma_f32_16x16x32_bf16 v[2:5], v[42:45], v[60:63], v[2:5]
	v_mfma_f32_16x16x32_bf16 v[2:5], v[50:53], v[38:41], v[2:5]
	s_waitcnt lgkmcnt(0)
	v_mfma_f32_16x16x32_bf16 v[2:5], v[64:67], v[46:49], v[2:5]
	v_mfma_f32_16x16x32_bf16 v[60:63], v[72:75], v[68:71], v[2:5]
	s_waitcnt lgkmcnt(0)
	v_cmp_gt_u32_e64 s[0:1], 16, v1
	v_cmp_lt_u32_e32 vcc, 15, v1
	s_waitcnt lgkmcnt(0)
	s_nop 2
	v_max_f32_e32 v2, v59, v59
	v_max_f32_e32 v3, v58, v58
	s_waitcnt lgkmcnt(0)
	v_max_f32_e32 v2, v3, v2
	s_nop 0
	s_nop 0
	s_nop 0
	s_waitcnt lgkmcnt(0)
	s_nop 0
	s_nop 0
	s_and_saveexec_b64 s[4:5], vcc
	s_xor_b64 s[4:5], exec, s[4:5]
	s_or_saveexec_b64 s[4:5], s[4:5]
	v_max3_f32 v53, v56, v57, v2
	s_xor_b64 exec, exec, s[4:5]
	v_max_f32_e32 v2, v61, v61
	v_max_f32_e32 v3, v60, v60
	v_max_f32_e32 v2, v3, v2
	v_max_f32_e32 v3, v63, v63
	v_max_f32_e32 v4, v62, v62
	v_max_f32_e32 v3, v4, v3
	v_max3_f32 v53, v53, v2, v3
	s_or_b64 exec, exec, s[4:5]
	v_cmp_eq_u32_e64 s[4:5], 1, v201
	v_max_f32_e32 v53, v53, v53
	v_mov_b32_e32 v68, v53
	s_nop 1
	v_permlane16_swap_b32_e32 v53, v68
	v_max_f32_e32 v68, v53, v68
	v_mov_b32_e32 v55, v68
	s_nop 1
	v_permlane32_swap_b32_e32 v68, v55
	v_max_f32_e32 v68, v68, v55
	v_sub_f32_e32 v55, v56, v68
	v_mul_f32_e32 v55, 0x3fb8aa3b, v55
	v_exp_f32_e32 v70, v55
	v_sub_f32_e32 v55, v57, v68
	v_sub_f32_e32 v57, v59, v68
	v_mul_f32_e32 v57, 0x3fb8aa3b, v57
	v_mul_f32_e32 v55, 0x3fb8aa3b, v55
	v_exp_f32_e32 v59, v57
	v_sub_f32_e32 v57, v60, v68
	v_exp_f32_e32 v71, v55
	v_sub_f32_e32 v55, v58, v68
	v_mul_f32_e32 v57, 0x3fb8aa3b, v57
	v_sub_f32_e32 v58, v61, v68
	v_exp_f32_e32 v57, v57
	v_mul_f32_e32 v58, 0x3fb8aa3b, v58
	v_exp_f32_e32 v58, v58
	v_mul_f32_e32 v55, 0x3fb8aa3b, v55
	v_exp_f32_e32 v72, v55
	v_cndmask_b32_e64 v60, 0, v57, s[0:1]
	v_sub_f32_e32 v57, v62, v68
	v_add_f32_e32 v56, 0, v70
	v_cndmask_b32_e64 v61, 0, v58, s[0:1]
	v_mul_f32_e32 v57, 0x3fb8aa3b, v57
	v_sub_f32_e32 v58, v63, v68
	v_add_f32_e32 v56, v56, v71
	v_exp_f32_e32 v57, v57
	v_mul_f32_e32 v58, 0x3fb8aa3b, v58
	v_add_f32_e32 v56, v56, v72
	v_exp_f32_e32 v58, v58
	v_add_f32_e32 v56, v56, v59
	v_add_f32_e32 v56, v56, v60
	v_add_f32_e32 v56, v56, v61
	v_cndmask_b32_e64 v62, 0, v57, s[0:1]
	v_add_f32_e32 v56, v56, v62
	v_cndmask_b32_e64 v63, 0, v58, s[0:1]
	v_add_f32_e32 v57, v56, v63
	v_mov_b32_e32 v58, v57
	s_nop 1
	v_permlane16_swap_b32_e32 v57, v58
	v_add_f32_e32 v58, v57, v58
	v_mov_b32_e32 v68, v58
	s_nop 1
	v_permlane32_swap_b32_e32 v58, v68
	v_add_f32_e32 v68, v58, v68
	v_div_scale_f32 v69, s[6:7], v68, v68, 1.0
	v_rcp_f32_e32 v73, v69
	s_nop 0
	v_fma_f32 v75, -v69, v73, 1.0
	v_fmac_f32_e32 v73, v75, v73
	v_div_scale_f32 v75, vcc, 1.0, v68, 1.0
	v_mul_f32_e32 v92, v75, v73
	v_fma_f32 v93, -v69, v92, v75
	v_fmac_f32_e32 v92, v93, v73
	v_fma_f32 v69, -v69, v92, v75
	v_div_fmas_f32 v69, v69, v73, v92
	v_div_fixup_f32 v68, v69, v68, 1.0
	v_mul_f32_e32 v69, v68, v70
	v_mov_b32_e32 v75, 0xbb23d70a
	v_mov_b32_e32 v73, 0x3b23d70a
	v_fmaak_f32 v92, v68, v70, 0xbb23d70a
	v_fmaak_f32 v70, v68, v70, 0x3b23d70a
	v_cmp_lt_f32_e32 vcc, v69, v75
	v_fmaak_f32 v93, v68, v60, 0xbb23d70a
	s_nop 0
	v_cndmask_b32_e32 v70, 0, v70, vcc
	v_cmp_gt_f32_e32 vcc, v69, v73
	s_nop 1
	v_cndmask_b32_e32 v69, v70, v92, vcc
	v_mul_f32_e32 v92, v68, v60
	v_fmaak_f32 v60, v68, v60, 0x3b23d70a
	v_cmp_lt_f32_e32 vcc, v92, v75
	v_max_f32_e32 v70, 0xf149f2ca, v69
	s_nop 0
	v_cndmask_b32_e32 v60, 0, v60, vcc
	v_cmp_gt_f32_e32 vcc, v92, v73
	s_nop 1
	v_cndmask_b32_e32 v92, v60, v93, vcc
	v_max_f32_e32 v60, v70, v92
	v_cndmask_b32_e64 v60, v70, v60, s[0:1]
	v_mul_f32_e32 v70, v68, v71
	v_fmaak_f32 v93, v68, v71, 0xbb23d70a
	v_fmaak_f32 v71, v68, v71, 0x3b23d70a
	v_cmp_lt_f32_e32 vcc, v70, v75
	s_nop 1
	v_cndmask_b32_e32 v71, 0, v71, vcc
	v_cmp_gt_f32_e32 vcc, v70, v73
	s_nop 1
	v_cndmask_b32_e32 v70, v71, v93, vcc
	v_mul_f32_e32 v71, v68, v61
	v_fmaak_f32 v93, v68, v61, 0xbb23d70a
	v_fmaak_f32 v61, v68, v61, 0x3b23d70a
	v_cmp_lt_f32_e32 vcc, v71, v75
	v_max_f32_e32 v60, v60, v70
	s_nop 0
	v_cndmask_b32_e32 v61, 0, v61, vcc
	v_cmp_gt_f32_e32 vcc, v71, v73
	s_nop 1
	v_cndmask_b32_e32 v71, v61, v93, vcc
	v_max_f32_e32 v61, v60, v71
	v_cndmask_b32_e64 v60, v60, v61, s[0:1]
	v_mul_f32_e32 v61, v68, v72
	v_fmaak_f32 v93, v68, v72, 0xbb23d70a
	v_fmaak_f32 v72, v68, v72, 0x3b23d70a
	v_cmp_lt_f32_e32 vcc, v61, v75
	s_nop 1
	v_cndmask_b32_e32 v72, 0, v72, vcc
	v_cmp_gt_f32_e32 vcc, v61, v73
	v_mul_f32_e32 v61, v68, v62
	s_nop 0
	v_cndmask_b32_e32 v72, v72, v93, vcc
	v_fmaak_f32 v93, v68, v62, 0xbb23d70a
	v_fmaak_f32 v62, v68, v62, 0x3b23d70a
	v_cmp_lt_f32_e32 vcc, v61, v75
	v_max_f32_e32 v60, v60, v72
	s_nop 0
	v_cndmask_b32_e32 v62, 0, v62, vcc
	v_cmp_gt_f32_e32 vcc, v61, v73
	s_nop 1
	v_cndmask_b32_e32 v62, v62, v93, vcc
	v_max_f32_e32 v61, v60, v62
	v_cndmask_b32_e64 v60, v60, v61, s[0:1]
	v_mul_f32_e32 v61, v68, v59
	v_fmaak_f32 v93, v68, v59, 0xbb23d70a
	v_fmaak_f32 v59, v68, v59, 0x3b23d70a
	v_cmp_lt_f32_e32 vcc, v61, v75
	s_nop 1
	v_cndmask_b32_e32 v59, 0, v59, vcc
	v_cmp_gt_f32_e32 vcc, v61, v73
	s_nop 1
	v_cndmask_b32_e32 v93, v59, v93, vcc
	v_max_f32_e32 v59, v60, v93
	v_mul_f32_e32 v60, v68, v63
	v_cmp_gt_f32_e32 vcc, v60, v73
	v_fmac_f32_e32 v73, v68, v63
	v_cmp_lt_f32_e64 s[6:7], v60, v75
	v_fmac_f32_e32 v75, v68, v63
	s_nop 0
	v_cndmask_b32_e64 v60, 0, v73, s[6:7]
	v_cndmask_b32_e32 v63, v60, v75, vcc
	v_max_f32_e32 v60, v59, v63
	v_cndmask_b32_e64 v60, v59, v60, s[0:1]
	v_mov_b32_e32 v61, v60
	s_nop 1
	v_permlane16_swap_b32_e32 v60, v61
	v_max_f32_e32 v61, v60, v61
	v_mov_b32_e32 v74, v61
	s_nop 1
	v_permlane32_swap_b32_e32 v61, v74
	v_max_f32_e32 v74, v61, v74
	v_sub_f32_e32 v61, v69, v74
	v_mul_f32_e32 v61, 0x3fb8aa3b, v61
	v_exp_f32_e32 v69, v61
	v_sub_f32_e32 v61, v92, v74
	v_mul_f32_e32 v61, 0x3fb8aa3b, v61
	v_exp_f32_e32 v75, v61
	v_sub_f32_e32 v70, v70, v74
	v_sub_f32_e32 v71, v71, v74
	v_mul_f32_e32 v70, 0x3fb8aa3b, v70
	v_mul_f32_e32 v71, 0x3fb8aa3b, v71
	v_exp_f32_e32 v70, v70
	v_exp_f32_e32 v71, v71
	v_sub_f32_e32 v72, v72, v74
	v_sub_f32_e32 v62, v62, v74
	v_mul_f32_e32 v72, 0x3fb8aa3b, v72
	v_mul_f32_e32 v62, 0x3fb8aa3b, v62
	v_add_f32_e32 v73, 0, v69
	v_cndmask_b32_e64 v75, 0, v75, s[0:1]
	v_exp_f32_e32 v72, v72
	v_exp_f32_e32 v62, v62
	v_sub_f32_e32 v84, v93, v74
	v_sub_f32_e32 v63, v63, v74
	v_add_f32_e32 v73, v73, v75
	v_mul_f32_e32 v84, 0x3fb8aa3b, v84
	v_mul_f32_e32 v63, 0x3fb8aa3b, v63
	v_add_f32_e32 v73, v73, v70
	v_cndmask_b32_e64 v71, 0, v71, s[0:1]
	v_exp_f32_e32 v84, v84
	v_exp_f32_e32 v63, v63
	v_add_f32_e32 v73, v73, v71
	v_add_f32_e32 v73, v73, v72
	v_cndmask_b32_e64 v74, 0, v62, s[0:1]
	v_add_f32_e32 v62, v73, v74
	v_add_f32_e32 v62, v62, v84
	v_cndmask_b32_e64 v73, 0, v63, s[0:1]
	v_add_f32_e32 v85, v62, v73
	v_mov_b32_e32 v66, v85
	s_nop 1
	v_permlane16_swap_b32_e32 v85, v66
	v_add_f32_e32 v66, v85, v66
	v_mov_b32_e32 v67, v66
	s_nop 1
	v_permlane32_swap_b32_e32 v66, v67
	v_add_f32_e32 v66, v66, v67
	v_div_scale_f32 v67, s[6:7], v66, v66, 1.0
	v_rcp_f32_e32 v78, v67
	s_nop 0
	v_fma_f32 v68, -v67, v78, 1.0
	v_fmac_f32_e32 v78, v68, v78
	v_div_scale_f32 v68, vcc, 1.0, v66, 1.0
	v_mul_f32_e32 v77, v68, v78
	v_fma_f32 v79, -v67, v77, v68
	v_fmac_f32_e32 v77, v79, v78
	v_fma_f32 v67, -v67, v77, v68
	v_div_fmas_f32 v67, v67, v78, v77
	v_div_fixup_f32 v66, v67, v66, 1.0
	v_mov_b32_e32 v67, 0xbd4ccccd
	v_fmaak_f32 v68, v66, v69, 0xbd4ccccd
	v_fmaak_f32 v69, v66, v70, 0xbd4ccccd
	v_fmaak_f32 v70, v66, v72, 0xbd4ccccd
	v_fmaak_f32 v75, v66, v75, 0xbd4ccccd
	v_fmaak_f32 v71, v66, v71, 0xbd4ccccd
	v_fmaak_f32 v74, v66, v74, 0xbd4ccccd
	v_mul_f32_e32 v70, 0x4038aa3b, v70
	v_fmaak_f32 v72, v66, v84, 0xbd4ccccd
	v_mul_f32_e32 v75, 0x4038aa3b, v75
	v_mul_f32_e32 v71, 0x4038aa3b, v71
	v_mul_f32_e32 v74, 0x4038aa3b, v74
	v_fmac_f32_e32 v67, v66, v73
	v_mul_f32_e32 v68, 0x4038aa3b, v68
	v_mul_f32_e32 v69, 0x4038aa3b, v69
	v_mul_f32_e32 v72, 0x4038aa3b, v72
	v_cndmask_b32_e64 v75, 0, v75, s[0:1]
	v_cndmask_b32_e64 v71, 0, v71, s[0:1]
	v_cndmask_b32_e64 v74, 0, v74, s[0:1]
	v_mul_f32_e32 v66, 0x4038aa3b, v67
	v_cvt_pk_bf16_f32 v67, v70, v72
	v_add_u32_e32 v70, v76, v198
	v_cndmask_b32_e64 v73, 0, v66, s[0:1]
	v_cndmask_b32_e64 v74, v74, 1.0, s[4:5]
	v_cndmask_b32_e64 v75, v75, 1.0, s[4:5]
	v_cndmask_b32_e64 v71, v71, 1.0, s[4:5]
	v_cvt_pk_bf16_f32 v66, v68, v69
	v_cvt_pk_bf16_f32 v68, v75, v71
	v_cvt_pk_bf16_f32 v69, v74, v73
	ds_write_b128 v70, v[66:69]
	s_movk_i32 s0, 0x210
	v_and_b32_e32 v67, 48, v0
	v_lshrrev_b32_e32 v0, 5, v1
	v_mad_u32_u24 v66, v197, s0, v199
	v_mad_u32_u24 v68, v0, s0, v199
	s_and_b32 s0, s2, 7
	s_lshl_b32 s0, s0, 22
	s_lshl_b32 s1, s3, 17
	v_lshlrev_b32_e32 v1, 13, v0
	s_add_i32 s0, s0, s1
	v_and_b32_e32 v69, 0x1f0, v194
	v_or3_b32 v1, s0, v1, v196
	s_mov_b32 s12, 0
	s_mov_b32 s11, 0x20000
	s_brev_b32 s10, 8
	s_and_b32 s9, s9, 0xffff
	v_or_b32_e32 v0, 0x24800, v198
	v_add_u32_e32 v1, v1, v69
	v_add_u32_e32 v106, v66, v67
	v_add_u32_e32 v107, v68, v69
	s_waitcnt lgkmcnt(0)
	s_barrier
.LBB0_3:
	ds_read_b128 v[70:73], v0
	v_add_u32_e32 v132, s12, v1
	v_add_u32_e32 v0, 0x400, v0
	v_add_u32_e32 v133, 0x4000, v132
	v_add_u32_e32 v134, 0x8000, v132
	v_add_u32_e32 v135, 0xc000, v132
	v_add_u32_e32 v136, 0x10000, v132
	v_add_u32_e32 v137, 0x14000, v132
	v_add_u32_e32 v138, 0x18000, v132
	v_add_u32_e32 v139, 0x1c000, v132
	s_waitcnt lgkmcnt(0)
	v_mfma_f32_16x16x32_bf16 v[74:77], v[144:147], v[70:73], 0
	v_mfma_f32_16x16x32_bf16 v[78:81], v[148:151], v[70:73], 0
	v_mfma_f32_16x16x32_bf16 v[82:85], v[152:155], v[70:73], 0
	v_mfma_f32_16x16x32_bf16 v[86:89], v[156:159], v[70:73], 0
	v_mfma_f32_16x16x32_bf16 v[90:93], v[160:163], v[70:73], 0
	v_mfma_f32_16x16x32_bf16 v[94:97], v[164:167], v[70:73], 0
	v_mfma_f32_16x16x32_bf16 v[98:101], v[168:171], v[70:73], 0
	v_mfma_f32_16x16x32_bf16 v[102:105], v[172:175], v[70:73], 0
	s_nop 0
	v_exp_f32_e32 v74, v74
	v_exp_f32_e32 v75, v75
	v_exp_f32_e32 v76, v76
	v_exp_f32_e32 v77, v77
	v_exp_f32_e32 v78, v78
	v_exp_f32_e32 v79, v79
	v_exp_f32_e32 v80, v80
	v_exp_f32_e32 v81, v81
	v_exp_f32_e32 v82, v82
	v_exp_f32_e32 v83, v83
	v_exp_f32_e32 v84, v84
	v_exp_f32_e32 v85, v85
	v_exp_f32_e32 v86, v86
	v_exp_f32_e32 v87, v87
	v_exp_f32_e32 v88, v88
	v_exp_f32_e32 v89, v89
	v_exp_f32_e32 v90, v90
	v_exp_f32_e32 v91, v91
	v_exp_f32_e32 v92, v92
	v_exp_f32_e32 v93, v93
	v_exp_f32_e32 v94, v94
	v_exp_f32_e32 v95, v95
	v_exp_f32_e32 v96, v96
	v_exp_f32_e32 v97, v97
	v_exp_f32_e32 v98, v98
	v_exp_f32_e32 v99, v99
	v_exp_f32_e32 v100, v100
	v_exp_f32_e32 v101, v101
	v_exp_f32_e32 v102, v102
	v_exp_f32_e32 v103, v103
	v_exp_f32_e32 v104, v104
	v_exp_f32_e32 v105, v105
	v_add_f32_e32 v74, 1.0, v74
	v_add_f32_e32 v75, 1.0, v75
	v_add_f32_e32 v76, 1.0, v76
	v_add_f32_e32 v77, 1.0, v77
	v_add_f32_e32 v78, 1.0, v78
	v_add_f32_e32 v79, 1.0, v79
	v_add_f32_e32 v80, 1.0, v80
	v_add_f32_e32 v81, 1.0, v81
	v_add_f32_e32 v82, 1.0, v82
	v_add_f32_e32 v83, 1.0, v83
	v_add_f32_e32 v84, 1.0, v84
	v_add_f32_e32 v85, 1.0, v85
	v_add_f32_e32 v86, 1.0, v86
	v_add_f32_e32 v87, 1.0, v87
	v_add_f32_e32 v88, 1.0, v88
	v_add_f32_e32 v89, 1.0, v89
	v_add_f32_e32 v90, 1.0, v90
	v_add_f32_e32 v91, 1.0, v91
	v_add_f32_e32 v92, 1.0, v92
	v_add_f32_e32 v93, 1.0, v93
	v_add_f32_e32 v94, 1.0, v94
	v_add_f32_e32 v95, 1.0, v95
	v_add_f32_e32 v96, 1.0, v96
	v_add_f32_e32 v97, 1.0, v97
	v_add_f32_e32 v98, 1.0, v98
	v_add_f32_e32 v99, 1.0, v99
	v_add_f32_e32 v100, 1.0, v100
	v_add_f32_e32 v101, 1.0, v101
	v_add_f32_e32 v102, 1.0, v102
	v_add_f32_e32 v103, 1.0, v103
	v_add_f32_e32 v104, 1.0, v104
	v_add_f32_e32 v105, 1.0, v105
	v_rcp_f32_e32 v74, v74
	v_rcp_f32_e32 v75, v75
	v_rcp_f32_e32 v76, v76
	v_rcp_f32_e32 v77, v77
	v_rcp_f32_e32 v78, v78
	v_rcp_f32_e32 v79, v79
	v_rcp_f32_e32 v80, v80
	v_rcp_f32_e32 v81, v81
	v_rcp_f32_e32 v82, v82
	v_rcp_f32_e32 v83, v83
	v_rcp_f32_e32 v84, v84
	v_rcp_f32_e32 v85, v85
	v_rcp_f32_e32 v86, v86
	v_rcp_f32_e32 v87, v87
	v_rcp_f32_e32 v88, v88
	v_rcp_f32_e32 v89, v89
	v_rcp_f32_e32 v90, v90
	v_rcp_f32_e32 v91, v91
	v_rcp_f32_e32 v92, v92
	v_rcp_f32_e32 v93, v93
	v_rcp_f32_e32 v94, v94
	v_rcp_f32_e32 v95, v95
	v_rcp_f32_e32 v96, v96
	v_rcp_f32_e32 v97, v97
	v_rcp_f32_e32 v98, v98
	v_rcp_f32_e32 v99, v99
	v_rcp_f32_e32 v100, v100
	v_rcp_f32_e32 v101, v101
	v_rcp_f32_e32 v102, v102
	v_rcp_f32_e32 v103, v103
	v_rcp_f32_e32 v104, v104
	v_rcp_f32_e32 v105, v105
	v_pk_fma_f32 v[74:75], v[74:75], -2.0, 1.0 op_sel_hi:[1,0,0]
	v_pk_fma_f32 v[76:77], v[76:77], -2.0, 1.0 op_sel_hi:[1,0,0]
	v_pk_fma_f32 v[78:79], v[78:79], -2.0, 1.0 op_sel_hi:[1,0,0]
	v_pk_fma_f32 v[80:81], v[80:81], -2.0, 1.0 op_sel_hi:[1,0,0]
	v_pk_fma_f32 v[82:83], v[82:83], -2.0, 1.0 op_sel_hi:[1,0,0]
	v_pk_fma_f32 v[84:85], v[84:85], -2.0, 1.0 op_sel_hi:[1,0,0]
	v_pk_fma_f32 v[86:87], v[86:87], -2.0, 1.0 op_sel_hi:[1,0,0]
	v_pk_fma_f32 v[88:89], v[88:89], -2.0, 1.0 op_sel_hi:[1,0,0]
	v_pk_fma_f32 v[90:91], v[90:91], -2.0, 1.0 op_sel_hi:[1,0,0]
	v_pk_fma_f32 v[92:93], v[92:93], -2.0, 1.0 op_sel_hi:[1,0,0]
	v_pk_fma_f32 v[94:95], v[94:95], -2.0, 1.0 op_sel_hi:[1,0,0]
	v_pk_fma_f32 v[96:97], v[96:97], -2.0, 1.0 op_sel_hi:[1,0,0]
	v_pk_fma_f32 v[98:99], v[98:99], -2.0, 1.0 op_sel_hi:[1,0,0]
	v_pk_fma_f32 v[100:101], v[100:101], -2.0, 1.0 op_sel_hi:[1,0,0]
	v_pk_fma_f32 v[102:103], v[102:103], -2.0, 1.0 op_sel_hi:[1,0,0]
	v_pk_fma_f32 v[104:105], v[104:105], -2.0, 1.0 op_sel_hi:[1,0,0]
	ds_write_b128 v106, v[74:77]
	ds_write_b128 v106, v[78:81] offset:64
	ds_write_b128 v106, v[82:85] offset:128
	ds_write_b128 v106, v[86:89] offset:192
	ds_write_b128 v106, v[90:93] offset:256
	ds_write_b128 v106, v[94:97] offset:320
	ds_write_b128 v106, v[98:101] offset:384
	ds_write_b128 v106, v[102:105] offset:448
	ds_read_b128 v[74:77], v107
	ds_read_b128 v[78:81], v107 offset:1056
	ds_read_b128 v[82:85], v107 offset:2112
	ds_read_b128 v[86:89], v107 offset:3168
	ds_read_b128 v[90:93], v107 offset:4224
	ds_read_b128 v[94:97], v107 offset:5280
	ds_read_b128 v[98:101], v107 offset:6336
	ds_read_b128 v[102:105], v107 offset:7392
	s_waitcnt lgkmcnt(7)
	buffer_store_dwordx4 v[74:77], v132, s[8:11], 0 offen sc0 nt sc1
	s_waitcnt lgkmcnt(6)
	buffer_store_dwordx4 v[78:81], v133, s[8:11], 0 offen sc0 nt sc1
	s_waitcnt lgkmcnt(5)
	buffer_store_dwordx4 v[82:85], v134, s[8:11], 0 offen sc0 nt sc1
	s_waitcnt lgkmcnt(4)
	buffer_store_dwordx4 v[86:89], v135, s[8:11], 0 offen sc0 nt sc1
	s_waitcnt lgkmcnt(3)
	buffer_store_dwordx4 v[90:93], v136, s[8:11], 0 offen sc0 nt sc1
	s_waitcnt lgkmcnt(2)
	buffer_store_dwordx4 v[94:97], v137, s[8:11], 0 offen sc0 nt sc1
	s_waitcnt lgkmcnt(1)
	buffer_store_dwordx4 v[98:101], v138, s[8:11], 0 offen sc0 nt sc1
	s_waitcnt lgkmcnt(0)
	buffer_store_dwordx4 v[102:105], v139, s[8:11], 0 offen sc0 nt sc1
	v_mfma_f32_16x16x32_bf16 v[74:77], v[176:179], v[70:73], 0
	v_mfma_f32_16x16x32_bf16 v[78:81], v[180:183], v[70:73], 0
	v_mfma_f32_16x16x32_bf16 v[82:85], v[184:187], v[70:73], 0
	v_mfma_f32_16x16x32_bf16 v[86:89], v[188:191], v[70:73], 0
	v_mfma_f32_16x16x32_bf16 v[90:93], v[232:235], v[70:73], 0
	v_mfma_f32_16x16x32_bf16 v[94:97], v[236:239], v[70:73], 0
	v_mfma_f32_16x16x32_bf16 v[98:101], v[240:243], v[70:73], 0
	v_mfma_f32_16x16x32_bf16 v[102:105], v[244:247], v[70:73], 0
	s_nop 0
	v_exp_f32_e32 v74, v74
	v_exp_f32_e32 v75, v75
	v_exp_f32_e32 v76, v76
	v_exp_f32_e32 v77, v77
	v_exp_f32_e32 v78, v78
	v_exp_f32_e32 v79, v79
	v_exp_f32_e32 v80, v80
	v_exp_f32_e32 v81, v81
	v_exp_f32_e32 v82, v82
	v_exp_f32_e32 v83, v83
	v_exp_f32_e32 v84, v84
	v_exp_f32_e32 v85, v85
	v_exp_f32_e32 v86, v86
	v_exp_f32_e32 v87, v87
	v_exp_f32_e32 v88, v88
	v_exp_f32_e32 v89, v89
	v_exp_f32_e32 v90, v90
	v_exp_f32_e32 v91, v91
	v_exp_f32_e32 v92, v92
	v_exp_f32_e32 v93, v93
	v_exp_f32_e32 v94, v94
	v_exp_f32_e32 v95, v95
	v_exp_f32_e32 v96, v96
	v_exp_f32_e32 v97, v97
	v_exp_f32_e32 v98, v98
	v_exp_f32_e32 v99, v99
	v_exp_f32_e32 v100, v100
	v_exp_f32_e32 v101, v101
	v_exp_f32_e32 v102, v102
	v_exp_f32_e32 v103, v103
	v_exp_f32_e32 v104, v104
	v_exp_f32_e32 v105, v105
	v_add_f32_e32 v74, 1.0, v74
	v_add_f32_e32 v75, 1.0, v75
	v_add_f32_e32 v76, 1.0, v76
	v_add_f32_e32 v77, 1.0, v77
	v_add_f32_e32 v78, 1.0, v78
	v_add_f32_e32 v79, 1.0, v79
	v_add_f32_e32 v80, 1.0, v80
	v_add_f32_e32 v81, 1.0, v81
	v_add_f32_e32 v82, 1.0, v82
	v_add_f32_e32 v83, 1.0, v83
	v_add_f32_e32 v84, 1.0, v84
	v_add_f32_e32 v85, 1.0, v85
	v_add_f32_e32 v86, 1.0, v86
	v_add_f32_e32 v87, 1.0, v87
	v_add_f32_e32 v88, 1.0, v88
	v_add_f32_e32 v89, 1.0, v89
	v_add_f32_e32 v90, 1.0, v90
	v_add_f32_e32 v91, 1.0, v91
	v_add_f32_e32 v92, 1.0, v92
	v_add_f32_e32 v93, 1.0, v93
	v_add_f32_e32 v94, 1.0, v94
	v_add_f32_e32 v95, 1.0, v95
	v_add_f32_e32 v96, 1.0, v96
	v_add_f32_e32 v97, 1.0, v97
	v_add_f32_e32 v98, 1.0, v98
	v_add_f32_e32 v99, 1.0, v99
	v_add_f32_e32 v100, 1.0, v100
	v_add_f32_e32 v101, 1.0, v101
	v_add_f32_e32 v102, 1.0, v102
	v_add_f32_e32 v103, 1.0, v103
	v_add_f32_e32 v104, 1.0, v104
	v_add_f32_e32 v105, 1.0, v105
	v_rcp_f32_e32 v74, v74
	v_rcp_f32_e32 v75, v75
	v_rcp_f32_e32 v76, v76
	v_rcp_f32_e32 v77, v77
	v_rcp_f32_e32 v78, v78
	v_rcp_f32_e32 v79, v79
	v_rcp_f32_e32 v80, v80
	v_rcp_f32_e32 v81, v81
	v_rcp_f32_e32 v82, v82
	v_rcp_f32_e32 v83, v83
	v_rcp_f32_e32 v84, v84
	v_rcp_f32_e32 v85, v85
	v_rcp_f32_e32 v86, v86
	v_rcp_f32_e32 v87, v87
	v_rcp_f32_e32 v88, v88
	v_rcp_f32_e32 v89, v89
	v_rcp_f32_e32 v90, v90
	v_rcp_f32_e32 v91, v91
	v_rcp_f32_e32 v92, v92
	v_rcp_f32_e32 v93, v93
	v_rcp_f32_e32 v94, v94
	v_rcp_f32_e32 v95, v95
	v_rcp_f32_e32 v96, v96
	v_rcp_f32_e32 v97, v97
	v_rcp_f32_e32 v98, v98
	v_rcp_f32_e32 v99, v99
	v_rcp_f32_e32 v100, v100
	v_rcp_f32_e32 v101, v101
	v_rcp_f32_e32 v102, v102
	v_rcp_f32_e32 v103, v103
	v_rcp_f32_e32 v104, v104
	v_rcp_f32_e32 v105, v105
	v_pk_fma_f32 v[74:75], v[74:75], -2.0, 1.0 op_sel_hi:[1,0,0]
	v_pk_fma_f32 v[76:77], v[76:77], -2.0, 1.0 op_sel_hi:[1,0,0]
	v_pk_fma_f32 v[78:79], v[78:79], -2.0, 1.0 op_sel_hi:[1,0,0]
	v_pk_fma_f32 v[80:81], v[80:81], -2.0, 1.0 op_sel_hi:[1,0,0]
	v_pk_fma_f32 v[82:83], v[82:83], -2.0, 1.0 op_sel_hi:[1,0,0]
	v_pk_fma_f32 v[84:85], v[84:85], -2.0, 1.0 op_sel_hi:[1,0,0]
	v_pk_fma_f32 v[86:87], v[86:87], -2.0, 1.0 op_sel_hi:[1,0,0]
	v_pk_fma_f32 v[88:89], v[88:89], -2.0, 1.0 op_sel_hi:[1,0,0]
	v_pk_fma_f32 v[90:91], v[90:91], -2.0, 1.0 op_sel_hi:[1,0,0]
	v_pk_fma_f32 v[92:93], v[92:93], -2.0, 1.0 op_sel_hi:[1,0,0]
	v_pk_fma_f32 v[94:95], v[94:95], -2.0, 1.0 op_sel_hi:[1,0,0]
	v_pk_fma_f32 v[96:97], v[96:97], -2.0, 1.0 op_sel_hi:[1,0,0]
	v_pk_fma_f32 v[98:99], v[98:99], -2.0, 1.0 op_sel_hi:[1,0,0]
	v_pk_fma_f32 v[100:101], v[100:101], -2.0, 1.0 op_sel_hi:[1,0,0]
	v_pk_fma_f32 v[102:103], v[102:103], -2.0, 1.0 op_sel_hi:[1,0,0]
	v_pk_fma_f32 v[104:105], v[104:105], -2.0, 1.0 op_sel_hi:[1,0,0]
	ds_write_b128 v106, v[74:77]
	ds_write_b128 v106, v[78:81] offset:64
	ds_write_b128 v106, v[82:85] offset:128
	ds_write_b128 v106, v[86:89] offset:192
	ds_write_b128 v106, v[90:93] offset:256
	ds_write_b128 v106, v[94:97] offset:320
	ds_write_b128 v106, v[98:101] offset:384
	ds_write_b128 v106, v[102:105] offset:448
	ds_read_b128 v[74:77], v107
	ds_read_b128 v[78:81], v107 offset:1056
	ds_read_b128 v[82:85], v107 offset:2112
	ds_read_b128 v[86:89], v107 offset:3168
	ds_read_b128 v[90:93], v107 offset:4224
	ds_read_b128 v[94:97], v107 offset:5280
	ds_read_b128 v[98:101], v107 offset:6336
	ds_read_b128 v[102:105], v107 offset:7392
	s_waitcnt lgkmcnt(7)
	buffer_store_dwordx4 v[74:77], v132, s[8:11], 0 offen offset:512 sc0 nt sc1
	s_waitcnt lgkmcnt(6)
	buffer_store_dwordx4 v[78:81], v133, s[8:11], 0 offen offset:512 sc0 nt sc1
	s_waitcnt lgkmcnt(5)
	buffer_store_dwordx4 v[82:85], v134, s[8:11], 0 offen offset:512 sc0 nt sc1
	s_waitcnt lgkmcnt(4)
	buffer_store_dwordx4 v[86:89], v135, s[8:11], 0 offen offset:512 sc0 nt sc1
	s_waitcnt lgkmcnt(3)
	buffer_store_dwordx4 v[90:93], v136, s[8:11], 0 offen offset:512 sc0 nt sc1
	s_waitcnt lgkmcnt(2)
	buffer_store_dwordx4 v[94:97], v137, s[8:11], 0 offen offset:512 sc0 nt sc1
	s_waitcnt lgkmcnt(1)
	buffer_store_dwordx4 v[98:101], v138, s[8:11], 0 offen offset:512 sc0 nt sc1
	s_waitcnt lgkmcnt(0)
	buffer_store_dwordx4 v[102:105], v139, s[8:11], 0 offen offset:512 sc0 nt sc1
	s_add_i32 s12, s12, 0x2000000
	s_cmp_eq_u32 s12, 0x10000000
	s_cbranch_scc0 .LBB0_3
	s_endpgm
